# P5 router logits: 16 butterflies batched hop by hop ahead of the compiler's own (which are kept as dummy-destination bpermutes with relaxed waits); P5 only
# baseline (speedup 1.0000x reference)
; template <bool COMBINE, bool ROUTE, bool FINAL, bool OUT8 = false, bool DUMMY = false> ...
;     ...
;         float ss = 0.f;
; #pragma unroll
;         for (int j = 0; j < 8; ++j) ss += xv[j].x * xv[j].x + xv[j].y * xv[j].y + xv[j].z * xv[j].z + xv[j].w * xv[j].w;
;         ss = wave_sum(ss);
;         const float rstd = 1.0f / sqrtf(ss * (1.f / D) + EPS);
;         if (FINAL) {
; #pragma unroll
;             for (int j = 0; j < 8; ++j) { const int c = 4 * lane + 256 * j; const f32x4 gv = *(const f32x4*)(g + c); *(f32x4*)(fout + (size_t)m * D + c) = xv[j] * rstd * gv; }
;         } else {
;             const float* sh = modl + (size_t)b * 12288 + sh_off; const float* sc = modl + (size_t)b * 12288 + sc_off;
; #pragma unroll
;             for (int j = 0; j < 8; ++j) {
;                 const int c = 4 * lane + 256 * j;
;                 const f32x4 gv = *(const f32x4*)(g + c), shv = *(const f32x4*)(sh + c), scv = *(const f32x4*)(sc + c);
;                 xv[j] = xv[j] * rstd * gv * (1.f + scv) + shv;
.LBB0_523:
	s_waitcnt vmcnt(7)
	v_mul_f32_e32 v0, v33, v33
	s_waitcnt vmcnt(6)
	v_mul_f32_e32 v1, v29, v29
	v_fmac_f32_e32 v0, v32, v32
	v_fmac_f32_e32 v1, v28, v28
	v_fmac_f32_e32 v0, v34, v34
	v_fmac_f32_e32 v1, v30, v30
	v_fmac_f32_e32 v0, v35, v35
	v_fmac_f32_e32 v1, v31, v31
	v_add_f32_e32 v0, v0, v1
	s_waitcnt vmcnt(5)
	v_mul_f32_e32 v1, v25, v25
	v_fmac_f32_e32 v1, v24, v24
	v_fmac_f32_e32 v1, v26, v26
	v_fmac_f32_e32 v1, v27, v27
	v_add_f32_e32 v0, v0, v1
	s_waitcnt vmcnt(4)
	v_mul_f32_e32 v1, v21, v21
	v_fmac_f32_e32 v1, v20, v20
	v_fmac_f32_e32 v1, v22, v22
	v_fmac_f32_e32 v1, v23, v23
	v_add_f32_e32 v0, v0, v1
	s_waitcnt vmcnt(3)
	v_mul_f32_e32 v1, v17, v17
	v_fmac_f32_e32 v1, v16, v16
	v_fmac_f32_e32 v1, v18, v18
	v_fmac_f32_e32 v1, v19, v19
	v_add_f32_e32 v0, v0, v1
	s_waitcnt vmcnt(2)
	v_mul_f32_e32 v1, v13, v13
	v_fmac_f32_e32 v1, v12, v12
	v_fmac_f32_e32 v1, v14, v14
	v_fmac_f32_e32 v1, v15, v15
	s_waitcnt vmcnt(1)
	v_mov_b32_e32 v74, v9
	s_waitcnt vmcnt(0)
	v_mov_b32_e32 v75, v5
	v_add_f32_e32 v59, v0, v1
	v_mov_b32_e32 v0, v8
	v_mov_b32_e32 v1, v4
	v_pk_mul_f32 v[74:75], v[74:75], v[74:75]
	v_lshl_add_u64 v[76:77], v[72:73], 0, s[54:55]
	v_pk_fma_f32 v[0:1], v[0:1], v[0:1], v[74:75]
	v_mov_b32_e32 v74, v10
	v_mov_b32_e32 v75, v6
	v_pk_fma_f32 v[0:1], v[74:75], v[74:75], v[0:1]
	v_mov_b32_e32 v74, v11
	v_mov_b32_e32 v75, v7
	v_pk_fma_f32 v[0:1], v[74:75], v[74:75], v[0:1]
	v_lshl_add_u64 v[74:75], v[72:73], 0, s[52:53]
	v_lshl_add_u64 v[72:73], v[74:75], 0, v[40:41]
	v_lshl_add_u64 v[164:165], v[76:77], 0, v[40:41]
	global_load_dwordx4 v[156:159], v[44:45], off
	global_load_dwordx4 v[160:163], v[72:73], off
	s_nop 0
	global_load_dwordx4 v[164:167], v[164:165], off
	global_load_dwordx4 v[168:171], v[44:45], off offset:1024
	v_mov_b32_e32 v172, v58
	v_mov_b32_e32 v173, 0
	v_lshl_add_u64 v[172:173], v[76:77], 0, v[172:173]
	global_load_dwordx4 v[172:175], v[172:173], off
	v_mov_b32_e32 v176, v58
	v_mov_b32_e32 v177, 0
	v_lshl_add_u64 v[176:177], v[74:75], 0, v[176:177]
	global_load_dwordx4 v[176:179], v[176:177], off
	global_load_dwordx4 v[180:183], v[44:45], off offset:2048
	v_mov_b32_e32 v184, v60
	v_mov_b32_e32 v185, 0
	v_lshl_add_u64 v[184:185], v[76:77], 0, v[184:185]
	global_load_dwordx4 v[184:187], v[184:185], off
	v_mov_b32_e32 v188, v60
	v_mov_b32_e32 v189, 0
	v_lshl_add_u64 v[188:189], v[74:75], 0, v[188:189]
	global_load_dwordx4 v[188:191], v[188:189], off
	global_load_dwordx4 v[192:195], v[44:45], off offset:3072
	v_mov_b32_e32 v196, v62
	v_mov_b32_e32 v197, 0
	v_lshl_add_u64 v[196:197], v[76:77], 0, v[196:197]
	global_load_dwordx4 v[196:199], v[196:197], off
	v_mov_b32_e32 v200, v62
	v_mov_b32_e32 v201, 0
	v_lshl_add_u64 v[200:201], v[74:75], 0, v[200:201]
	global_load_dwordx4 v[200:203], v[200:201], off
	global_load_dwordx4 v[204:207], v[46:47], off
	v_mov_b32_e32 v208, v64
	v_mov_b32_e32 v209, 0
	v_lshl_add_u64 v[208:209], v[76:77], 0, v[208:209]
	global_load_dwordx4 v[208:211], v[208:209], off
	v_mov_b32_e32 v212, v64
	v_mov_b32_e32 v213, 0
	v_lshl_add_u64 v[212:213], v[74:75], 0, v[212:213]
	global_load_dwordx4 v[212:215], v[212:213], off
	global_load_dwordx4 v[216:219], v[48:49], off
	v_mov_b32_e32 v220, v66
	v_mov_b32_e32 v221, 0
	v_lshl_add_u64 v[220:221], v[76:77], 0, v[220:221]
	global_load_dwordx4 v[220:223], v[220:221], off
	v_mov_b32_e32 v224, v66
	v_mov_b32_e32 v225, 0
	v_lshl_add_u64 v[224:225], v[74:75], 0, v[224:225]
	global_load_dwordx4 v[224:227], v[224:225], off
	global_load_dwordx4 v[228:231], v[50:51], off
	v_mov_b32_e32 v246, v68
	v_mov_b32_e32 v247, 0
	v_lshl_add_u64 v[246:247], v[76:77], 0, v[246:247]
	global_load_dwordx4 v[246:249], v[246:247], off
	v_mov_b32_e32 v250, v68
	v_mov_b32_e32 v251, 0
	v_lshl_add_u64 v[250:251], v[74:75], 0, v[250:251]
	global_load_dwordx4 v[250:253], v[250:251], off
	global_load_dwordx4 v[232:235], v[52:53], off
	v_mov_b32_e32 v236, v70
	v_mov_b32_e32 v237, 0
	v_lshl_add_u64 v[236:237], v[74:75], 0, v[236:237]
	global_load_dwordx4 v[236:239], v[236:237], off
	v_mov_b32_e32 v242, v70
	v_mov_b32_e32 v243, 0
	v_lshl_add_u64 v[242:243], v[76:77], 0, v[242:243]
	global_load_dwordx4 v[242:245], v[242:243], off
	v_add_f32_e32 v0, v59, v0
	v_add_f32_e32 v0, v0, v1
	ds_bpermute_b32 v1, v78, v0
	v_mov_b32_e32 v65, v41
	v_mov_b32_e32 v67, v41
	v_mov_b32_e32 v69, v41
	v_mov_b32_e32 v71, v41
	s_waitcnt lgkmcnt(0)
	v_add_f32_e32 v0, v0, v1
	ds_bpermute_b32 v1, v79, v0
	s_waitcnt lgkmcnt(0)
	v_add_f32_e32 v0, v0, v1
	ds_bpermute_b32 v1, v80, v0
	s_waitcnt lgkmcnt(0)
	v_add_f32_e32 v0, v0, v1
	ds_bpermute_b32 v1, v81, v0
	s_waitcnt lgkmcnt(0)
	v_add_f32_e32 v0, v0, v1
	ds_bpermute_b32 v1, v82, v0
	s_waitcnt lgkmcnt(0)
	v_add_f32_e32 v0, v0, v1
	ds_bpermute_b32 v1, v83, v0
	s_waitcnt lgkmcnt(0)
	v_add_f32_e32 v0, v0, v1
	v_fmamk_f32 v0, v0, 0x3a000000, v39
	v_mul_f32_e32 v1, 0x4f800000, v0
	v_cmp_gt_f32_e32 vcc, s3, v0
	s_waitcnt vmcnt(0)
; __device__ __forceinline__ unsigned pk2(float a, float b) { f32x2 v = {a, b}; bf16x2_t r = __builtin_convertvector(v, bf16x2_t); return __builtin_bit_cast(unsigned, r); }
; __device__ __forceinline__ unsigned pk4_fp8(float a, float b, float c, float d) { unsigned w = 0u; w = __builtin_amdgcn_cvt_pk_fp8_f32(a, b, w, false); w = __builtin_amdgcn_cvt_pk_fp8_f32(c, d, w, true); return w; }
; template <bool COMBINE, bool ROUTE, bool FINAL, bool OUT8 = false, bool DUMMY = false> ...
;     ...
;         const float rstd = 1.0f / sqrtf(ss * (1.f / D) + EPS);
;         if (FINAL) {
; #pragma unroll
;             for (int j = 0; j < 8; ++j) { const int c = 4 * lane + 256 * j; const f32x4 gv = *(const f32x4*)(g + c); *(f32x4*)(fout + (size_t)m * D + c) = xv[j] * rstd * gv; }
;         } else {
;             const float* sh = modl + (size_t)b * 12288 + sh_off; const float* sc = modl + (size_t)b * 12288 + sc_off;
; #pragma unroll
;             for (int j = 0; j < 8; ++j) {
;                 const int c = 4 * lane + 256 * j;
;                 const f32x4 gv = *(const f32x4*)(g + c), shv = *(const f32x4*)(sh + c), scv = *(const f32x4*)(sc + c);
;                 xv[j] = xv[j] * rstd * gv * (1.f + scv) + shv;
;                 if (OUT8) *(unsigned*)((unsigned char*)hout + (size_t)m * D + c) = pk4_fp8(xv[j].x * F8_SA, xv[j].y * F8_SA, xv[j].z * F8_SA, xv[j].w * F8_SA);
;                 else { u32x2 o; o.x = pk2(xv[j].x, xv[j].y); o.y = pk2(xv[j].z, xv[j].w); *(u32x2*)(hout + (size_t)m * D + c) = o; }
	v_pk_add_f32 v[72:73], v[164:165], 1.0 op_sel_hi:[1,0]
	v_cndmask_b32_e32 v0, v0, v1, vcc
	v_sqrt_f32_e32 v1, v0
	s_nop 0
	v_add_u32_e32 v40, -1, v1
	v_fma_f32 v59, -v40, v1, v0
	v_cmp_ge_f32_e64 s[6:7], 0, v59
	v_add_u32_e32 v59, 1, v1
	s_nop 0
	v_cndmask_b32_e64 v40, v1, v40, s[6:7]
	v_fma_f32 v1, -v59, v1, v0
	v_cmp_lt_f32_e64 s[6:7], 0, v1
	s_nop 1
	v_cndmask_b32_e64 v1, v40, v59, s[6:7]
	v_mul_f32_e32 v40, 0x37800000, v1
	v_cndmask_b32_e32 v1, v1, v40, vcc
	v_cmp_class_f32_e32 vcc, v0, v150
	s_nop 1
	v_cndmask_b32_e32 v0, v1, v0, vcc
	v_div_scale_f32 v1, s[6:7], v0, v0, 1.0
	v_rcp_f32_e32 v40, v1
	s_nop 0
	v_fma_f32 v59, -v1, v40, 1.0
	v_fmac_f32_e32 v40, v59, v40
	v_div_scale_f32 v59, vcc, 1.0, v0, 1.0
	v_mul_f32_e32 v61, v59, v40
	v_fma_f32 v63, -v1, v61, v59
	v_fmac_f32_e32 v61, v63, v40
	v_fma_f32 v1, -v1, v61, v59
	v_div_fmas_f32 v1, v1, v40, v61
	v_div_fixup_f32 v40, v1, v0, 1.0
	v_pk_mul_f32 v[32:33], v[32:33], v[40:41] op_sel_hi:[1,0]
	v_mov_b32_e32 v59, v41
	v_pk_mul_f32 v[32:33], v[156:157], v[32:33]
	v_pk_mul_f32 v[0:1], v[34:35], v[40:41] op_sel_hi:[1,0]
	v_pk_fma_f32 v[72:73], v[72:73], v[32:33], v[160:161]
	v_pk_mul_f32 v[0:1], v[158:159], v[0:1]
	v_mul_f32_e32 v32, 0x41800000, v72
	v_mul_f32_e32 v33, 0x41800000, v73
	v_cvt_pk_fp8_f32 v59, v32, v33
	v_pk_add_f32 v[34:35], v[166:167], 1.0 op_sel_hi:[1,0]
	v_pk_mul_f32 v[28:29], v[28:29], v[40:41] op_sel_hi:[1,0]
	v_pk_fma_f32 v[32:33], v[34:35], v[0:1], v[162:163]
	v_mov_b32_e32 v61, v41
	v_mul_f32_e32 v0, 0x41800000, v32
	v_mul_f32_e32 v1, 0x41800000, v33
	v_cvt_pk_fp8_f32 v59, v0, v1 op_sel:[0,0,1]
	v_lshlrev_b64 v[0:1], 11, v[2:3]
	v_lshl_add_u64 v[34:35], v[56:57], 0, v[0:1]
	v_mov_b32_e32 v3, v41
	global_store_dword v[34:35], v59, off
	v_mov_b32_e32 v59, v41
	v_lshl_add_u64 v[0:1], v[76:77], 0, v[58:59]
	v_lshl_add_u64 v[0:1], v[74:75], 0, v[58:59]
	v_pk_mul_f32 v[0:1], v[30:31], v[40:41] op_sel_hi:[1,0]
	v_pk_mul_f32 v[24:25], v[24:25], v[40:41] op_sel_hi:[1,0]
	v_mov_b32_e32 v63, v41
	v_pk_mul_f32 v[20:21], v[20:21], v[40:41] op_sel_hi:[1,0]
	v_pk_mul_f32 v[16:17], v[16:17], v[40:41] op_sel_hi:[1,0]
	v_pk_mul_f32 v[12:13], v[12:13], v[40:41] op_sel_hi:[1,0]
	v_pk_mul_f32 v[8:9], v[8:9], v[40:41] op_sel_hi:[1,0]
	v_pk_mul_f32 v[6:7], v[6:7], v[40:41] op_sel_hi:[1,0]
	v_pk_mul_f32 v[4:5], v[4:5], v[40:41] op_sel_hi:[1,0]
	v_pk_mul_f32 v[28:29], v[168:169], v[28:29]
	v_pk_add_f32 v[30:31], v[172:173], 1.0 op_sel_hi:[1,0]
	v_pk_mul_f32 v[0:1], v[170:171], v[0:1]
	v_pk_fma_f32 v[30:31], v[30:31], v[28:29], v[176:177]
	v_pk_add_f32 v[156:157], v[174:175], 1.0 op_sel_hi:[1,0]
	v_mul_f32_e32 v28, 0x41800000, v30
	v_mul_f32_e32 v29, 0x41800000, v31
	v_cvt_pk_fp8_f32 v3, v28, v29
	v_pk_fma_f32 v[28:29], v[156:157], v[0:1], v[178:179]
	s_nop 0
	v_mul_f32_e32 v0, 0x41800000, v28
	v_mul_f32_e32 v1, 0x41800000, v29
	v_cvt_pk_fp8_f32 v3, v0, v1 op_sel:[0,0,1]
	v_lshl_add_u64 v[0:1], v[76:77], 0, v[60:61]
	global_store_dword v[34:35], v3, off offset:256
	v_lshl_add_u64 v[0:1], v[74:75], 0, v[60:61]
	v_pk_mul_f32 v[0:1], v[26:27], v[40:41] op_sel_hi:[1,0]
	v_mov_b32_e32 v3, v41
	v_pk_mul_f32 v[24:25], v[180:181], v[24:25]
	v_pk_add_f32 v[26:27], v[184:185], 1.0 op_sel_hi:[1,0]
	v_pk_mul_f32 v[0:1], v[182:183], v[0:1]
	v_pk_fma_f32 v[26:27], v[24:25], v[26:27], v[188:189]
	v_pk_add_f32 v[156:157], v[186:187], 1.0 op_sel_hi:[1,0]
	v_mul_f32_e32 v24, 0x41800000, v26
	v_mul_f32_e32 v25, 0x41800000, v27
	v_cvt_pk_fp8_f32 v3, v24, v25
	v_pk_fma_f32 v[24:25], v[0:1], v[156:157], v[190:191]
	s_nop 0
	v_mul_f32_e32 v0, 0x41800000, v24
	v_mul_f32_e32 v1, 0x41800000, v25
	v_cvt_pk_fp8_f32 v3, v0, v1 op_sel:[0,0,1]
	v_lshl_add_u64 v[0:1], v[76:77], 0, v[62:63]
	global_store_dword v[34:35], v3, off offset:512
	v_lshl_add_u64 v[0:1], v[74:75], 0, v[62:63]
	v_pk_mul_f32 v[0:1], v[22:23], v[40:41] op_sel_hi:[1,0]
	v_mov_b32_e32 v3, v41
	v_pk_mul_f32 v[20:21], v[20:21], v[192:193]
	v_pk_add_f32 v[22:23], v[196:197], 1.0 op_sel_hi:[1,0]
	v_pk_mul_f32 v[0:1], v[0:1], v[194:195]
	v_pk_fma_f32 v[22:23], v[20:21], v[22:23], v[200:201]
	v_pk_add_f32 v[156:157], v[198:199], 1.0 op_sel_hi:[1,0]
	v_mul_f32_e32 v20, 0x41800000, v22
	v_mul_f32_e32 v21, 0x41800000, v23
	v_cvt_pk_fp8_f32 v3, v20, v21
	v_pk_fma_f32 v[20:21], v[0:1], v[156:157], v[202:203]
	s_nop 0
	v_mul_f32_e32 v0, 0x41800000, v20
	v_mul_f32_e32 v1, 0x41800000, v21
	v_cvt_pk_fp8_f32 v3, v0, v1 op_sel:[0,0,1]
	v_lshl_add_u64 v[0:1], v[76:77], 0, v[64:65]
	global_store_dword v[34:35], v3, off offset:768
	v_lshl_add_u64 v[0:1], v[74:75], 0, v[64:65]
	v_pk_mul_f32 v[0:1], v[18:19], v[40:41] op_sel_hi:[1,0]
	v_mov_b32_e32 v3, v41
	v_pk_mul_f32 v[16:17], v[16:17], v[204:205]
	v_pk_add_f32 v[18:19], v[208:209], 1.0 op_sel_hi:[1,0]
	v_pk_mul_f32 v[0:1], v[0:1], v[206:207]
	v_pk_fma_f32 v[18:19], v[16:17], v[18:19], v[212:213]
	v_pk_add_f32 v[156:157], v[210:211], 1.0 op_sel_hi:[1,0]
	v_mul_f32_e32 v16, 0x41800000, v18
	v_mul_f32_e32 v17, 0x41800000, v19
	v_cvt_pk_fp8_f32 v3, v16, v17
	v_pk_fma_f32 v[16:17], v[0:1], v[156:157], v[214:215]
	s_nop 0
	v_mul_f32_e32 v0, 0x41800000, v16
	v_mul_f32_e32 v1, 0x41800000, v17
	v_cvt_pk_fp8_f32 v3, v0, v1 op_sel:[0,0,1]
	v_lshl_add_u64 v[0:1], v[76:77], 0, v[66:67]
	global_store_dword v[34:35], v3, off offset:1024
	v_lshl_add_u64 v[0:1], v[74:75], 0, v[66:67]
	v_pk_mul_f32 v[0:1], v[14:15], v[40:41] op_sel_hi:[1,0]
	v_mov_b32_e32 v3, v41
	v_pk_mul_f32 v[12:13], v[12:13], v[216:217]
	v_pk_add_f32 v[14:15], v[220:221], 1.0 op_sel_hi:[1,0]
	v_pk_mul_f32 v[0:1], v[0:1], v[218:219]
	v_pk_fma_f32 v[14:15], v[12:13], v[14:15], v[224:225]
	v_pk_add_f32 v[156:157], v[222:223], 1.0 op_sel_hi:[1,0]
	v_mul_f32_e32 v12, 0x41800000, v14
; __device__ __forceinline__ unsigned pk2(float a, float b) { f32x2 v = {a, b}; bf16x2_t r = __builtin_convertvector(v, bf16x2_t); return __builtin_bit_cast(unsigned, r); }
; __device__ __forceinline__ unsigned pk4_fp8(float a, float b, float c, float d) { unsigned w = 0u; w = __builtin_amdgcn_cvt_pk_fp8_f32(a, b, w, false); w = __builtin_amdgcn_cvt_pk_fp8_f32(c, d, w, true); return w; }
; template <bool COMBINE, bool ROUTE, bool FINAL, bool OUT8 = false, bool DUMMY = false> ...
;     ...
;                 if (OUT8) *(unsigned*)((unsigned char*)hout + (size_t)m * D + c) = pk4_fp8(xv[j].x * F8_SA, xv[j].y * F8_SA, xv[j].z * F8_SA, xv[j].w * F8_SA);
;                 else { u32x2 o; o.x = pk2(xv[j].x, xv[j].y); o.y = pk2(xv[j].z, xv[j].w); *(u32x2*)(hout + (size_t)m * D + c) = o; }
;             }
;             if (ROUTE) {
;                 float lg[16];
; #pragma unroll
;                 for (int e = 0; e < 16; ++e) lg[e] = 0.f;
; #pragma unroll
;                 for (int j = 0; j < 8; ++j) {
; #pragma unroll
;                     for (int cc = 0; cc < 4; ++cc) {
;                         const float hv = xv[j][cc];
;                         const f32x4 w0 = WT[((j * 4 + cc) * 4 + 0) * 64 + lane], w1 = WT[((j * 4 + cc) * 4 + 1) * 64 + lane], w2 = WT[((j * 4 + cc) * 4 + 2) * 64 + lane], w3 = WT[((j * 4 + cc) * 4 + 3) * 64 + lane];
;                         lg[0] += hv * w0.x; lg[1] += hv * w0.y; lg[2] += hv * w0.z; lg[3] += hv * w0.w;
;                         lg[4] += hv * w1.x; lg[5] += hv * w1.y; lg[6] += hv * w1.z; lg[7] += hv * w1.w;
;                         lg[8] += hv * w2.x; lg[9] += hv * w2.y; lg[10] += hv * w2.z; lg[11] += hv * w2.w;
;                         lg[12] += hv * w3.x; lg[13] += hv * w3.y; lg[14] += hv * w3.z; lg[15] += hv * w3.w;
;                     }
;                     __builtin_amdgcn_sched_barrier(0);
;                 }
	v_mul_f32_e32 v13, 0x41800000, v15
	v_cvt_pk_fp8_f32 v3, v12, v13
	v_pk_fma_f32 v[12:13], v[0:1], v[156:157], v[226:227]
	s_nop 0
	v_mul_f32_e32 v0, 0x41800000, v12
	v_mul_f32_e32 v1, 0x41800000, v13
	v_cvt_pk_fp8_f32 v3, v0, v1 op_sel:[0,0,1]
	v_lshl_add_u64 v[0:1], v[76:77], 0, v[68:69]
	global_store_dword v[34:35], v3, off offset:1280
	v_lshl_add_u64 v[0:1], v[74:75], 0, v[68:69]
	v_pk_mul_f32 v[0:1], v[10:11], v[40:41] op_sel_hi:[1,0]
	v_mov_b32_e32 v3, v41
	v_pk_mul_f32 v[8:9], v[8:9], v[228:229]
	v_pk_add_f32 v[10:11], v[246:247], 1.0 op_sel_hi:[1,0]
	v_pk_mul_f32 v[0:1], v[0:1], v[230:231]
	v_pk_fma_f32 v[10:11], v[8:9], v[10:11], v[250:251]
	v_pk_add_f32 v[156:157], v[248:249], 1.0 op_sel_hi:[1,0]
	v_mul_f32_e32 v8, 0x41800000, v10
	v_mul_f32_e32 v9, 0x41800000, v11
	v_cvt_pk_fp8_f32 v3, v8, v9
	v_pk_fma_f32 v[8:9], v[0:1], v[156:157], v[252:253]
	v_mov_b32_e32 v157, v41
	v_mul_f32_e32 v0, 0x41800000, v8
	v_mul_f32_e32 v1, 0x41800000, v9
	v_cvt_pk_fp8_f32 v3, v0, v1 op_sel:[0,0,1]
	v_lshl_add_u64 v[0:1], v[74:75], 0, v[70:71]
	v_lshl_add_u64 v[74:75], v[76:77], 0, v[70:71]
	global_store_dword v[34:35], v3, off offset:1536
	ds_read_b128 v[74:77], v84
	ds_read_b128 v[170:173], v84 offset:1024
	ds_read_b128 v[174:177], v84 offset:2048
	ds_read_b128 v[178:181], v84 offset:3072
	ds_read_b128 v[182:185], v84 offset:4096
	ds_read_b128 v[186:189], v84 offset:5120
	ds_read_b128 v[190:193], v84 offset:6144
	ds_read_b128 v[194:197], v84 offset:7168
	ds_read_b128 v[198:201], v84 offset:8192
	ds_read_b128 v[202:205], v84 offset:9216
	ds_read_b128 v[206:209], v84 offset:10240
	ds_read_b128 v[210:213], v84 offset:11264
	ds_read_b128 v[214:217], v84 offset:12288
	ds_read_b128 v[218:221], v84 offset:13312
	ds_read_b128 v[224:227], v84 offset:14336
	ds_read_b128 v[228:231], v84 offset:15360
	s_waitcnt lgkmcnt(14)
	v_fma_f32 v156, v72, v74, 0
	v_fma_f32 v155, v72, v75, 0
	v_fma_f32 v67, v72, v76, 0
	v_fma_f32 v65, v72, v77, 0
	v_fma_f32 v77, v72, v170, 0
	v_fma_f32 v76, v72, v171, 0
	v_fma_f32 v63, v72, v172, 0
	v_fma_f32 v61, v72, v173, 0
	s_waitcnt lgkmcnt(13)
	v_fma_f32 v75, v72, v174, 0
	v_fma_f32 v74, v72, v175, 0
	v_fma_f32 v59, v72, v176, 0
	v_fma_f32 v40, v72, v177, 0
	s_waitcnt lgkmcnt(12)
	v_fma_f32 v71, v72, v178, 0
	v_fma_f32 v69, v72, v179, 0
	v_fma_f32 v3, v72, v180, 0
	v_fma_f32 v1, v72, v181, 0
	s_waitcnt lgkmcnt(11)
	v_fmac_f32_e32 v156, v73, v182
	v_fmac_f32_e32 v155, v73, v183
	v_fmac_f32_e32 v67, v73, v184
	v_fmac_f32_e32 v65, v73, v185
	s_waitcnt lgkmcnt(10)
	v_fmac_f32_e32 v77, v73, v186
	v_fmac_f32_e32 v76, v73, v187
	v_fmac_f32_e32 v63, v73, v188
	v_fmac_f32_e32 v61, v73, v189
	s_waitcnt lgkmcnt(9)
	v_fmac_f32_e32 v75, v73, v190
	v_fmac_f32_e32 v74, v73, v191
	v_fmac_f32_e32 v59, v73, v192
	v_fmac_f32_e32 v40, v73, v193
	s_waitcnt lgkmcnt(8)
	v_fmac_f32_e32 v71, v73, v194
	v_fmac_f32_e32 v69, v73, v195
	v_fmac_f32_e32 v3, v73, v196
	v_fmac_f32_e32 v1, v73, v197
	s_waitcnt lgkmcnt(7)
	v_fmac_f32_e32 v156, v32, v198
	v_fmac_f32_e32 v155, v32, v199
	v_fmac_f32_e32 v67, v32, v200
	v_fmac_f32_e32 v65, v32, v201
	s_waitcnt lgkmcnt(6)
	v_fmac_f32_e32 v77, v32, v202
	v_fmac_f32_e32 v76, v32, v203
	v_fmac_f32_e32 v63, v32, v204
	v_fmac_f32_e32 v61, v32, v205
	s_waitcnt lgkmcnt(5)
	v_fmac_f32_e32 v75, v32, v206
	v_fmac_f32_e32 v74, v32, v207
	v_fmac_f32_e32 v59, v32, v208
	v_fmac_f32_e32 v40, v32, v209
	s_waitcnt lgkmcnt(4)
	v_fmac_f32_e32 v71, v32, v210
	v_fmac_f32_e32 v69, v32, v211
	v_fmac_f32_e32 v3, v32, v212
	v_fmac_f32_e32 v1, v32, v213
	s_waitcnt lgkmcnt(1)
	v_fmac_f32_e32 v59, v33, v226
	v_fmac_f32_e32 v40, v33, v227
	s_waitcnt lgkmcnt(0)
	v_fmac_f32_e32 v3, v33, v230
	v_fmac_f32_e32 v1, v33, v231
	v_fmac_f32_e32 v156, v33, v214
	v_fmac_f32_e32 v155, v33, v215
	v_fmac_f32_e32 v67, v33, v216
	v_fmac_f32_e32 v65, v33, v217
	v_fmac_f32_e32 v77, v33, v218
	v_fmac_f32_e32 v76, v33, v219
	v_fmac_f32_e32 v63, v33, v220
	v_fmac_f32_e32 v61, v33, v221
	v_fmac_f32_e32 v75, v33, v224
	v_fmac_f32_e32 v74, v33, v225
	v_fmac_f32_e32 v71, v33, v228
	v_fmac_f32_e32 v69, v33, v229
	v_pk_mul_f32 v[4:5], v[4:5], v[232:233]
	v_pk_mul_f32 v[72:73], v[6:7], v[234:235]
	v_pk_add_f32 v[6:7], v[242:243], 1.0 op_sel_hi:[1,0]
	v_pk_add_f32 v[158:159], v[244:245], 1.0 op_sel_hi:[1,0]
	v_pk_fma_f32 v[6:7], v[4:5], v[6:7], v[236:237]
	s_nop 0
	v_mul_f32_e32 v0, 0x41800000, v6
	v_mul_f32_e32 v4, 0x41800000, v7
	v_cvt_pk_fp8_f32 v157, v0, v4
	v_pk_fma_f32 v[4:5], v[72:73], v[158:159], v[238:239]
	s_nop 0
	v_mul_f32_e32 v0, 0x41800000, v4
	v_mul_f32_e32 v32, 0x41800000, v5
	v_cvt_pk_fp8_f32 v157, v0, v32 op_sel:[0,0,1]
	global_store_dword v[34:35], v157, off offset:1792
	ds_read_b128 v[32:35], v84 offset:16384
	ds_read_b128 v[158:161], v84 offset:17408
	ds_read_b128 v[162:165], v84 offset:18432
	ds_read_b128 v[166:169], v84 offset:19456
	s_waitcnt lgkmcnt(3)
	v_fmac_f32_e32 v156, v30, v32
	v_fmac_f32_e32 v155, v30, v33
	v_fmac_f32_e32 v67, v30, v34
	v_fmac_f32_e32 v65, v30, v35
	s_waitcnt lgkmcnt(2)
	v_fmac_f32_e32 v77, v30, v158
	v_fmac_f32_e32 v76, v30, v159
	v_fmac_f32_e32 v63, v30, v160
	v_fmac_f32_e32 v61, v30, v161
	s_waitcnt lgkmcnt(1)
	v_fmac_f32_e32 v75, v30, v162
	v_fmac_f32_e32 v74, v30, v163
	v_fmac_f32_e32 v59, v30, v164
	v_fmac_f32_e32 v40, v30, v165
	s_waitcnt lgkmcnt(0)
	v_fmac_f32_e32 v71, v30, v166
	v_fmac_f32_e32 v69, v30, v167
	v_fmac_f32_e32 v3, v30, v168
	ds_read_b128 v[32:35], v84 offset:20480
	v_fmac_f32_e32 v1, v30, v169
	ds_read_b128 v[158:161], v84 offset:21504
	ds_read_b128 v[162:165], v84 offset:22528
	ds_read_b128 v[166:169], v84 offset:23552
	s_waitcnt lgkmcnt(3)
; template <bool COMBINE, bool ROUTE, bool FINAL, bool OUT8 = false, bool DUMMY = false> ...
;     ...
;                 for (int j = 0; j < 8; ++j) {
; #pragma unroll
;                     for (int cc = 0; cc < 4; ++cc) {
;                         const float hv = xv[j][cc];
;                         const f32x4 w0 = WT[((j * 4 + cc) * 4 + 0) * 64 + lane], w1 = WT[((j * 4 + cc) * 4 + 1) * 64 + lane], w2 = WT[((j * 4 + cc) * 4 + 2) * 64 + lane], w3 = WT[((j * 4 + cc) * 4 + 3) * 64 + lane];
;                         lg[0] += hv * w0.x; lg[1] += hv * w0.y; lg[2] += hv * w0.z; lg[3] += hv * w0.w;
;                         lg[4] += hv * w1.x; lg[5] += hv * w1.y; lg[6] += hv * w1.z; lg[7] += hv * w1.w;
;                         lg[8] += hv * w2.x; lg[9] += hv * w2.y; lg[10] += hv * w2.z; lg[11] += hv * w2.w;
;                         lg[12] += hv * w3.x; lg[13] += hv * w3.y; lg[14] += hv * w3.z; lg[15] += hv * w3.w;
;                     }
	v_fmac_f32_e32 v156, v31, v32
	v_fmac_f32_e32 v155, v31, v33
	v_fmac_f32_e32 v67, v31, v34
	v_fmac_f32_e32 v65, v31, v35
	s_waitcnt lgkmcnt(2)
	v_fmac_f32_e32 v77, v31, v158
	v_fmac_f32_e32 v76, v31, v159
	v_fmac_f32_e32 v63, v31, v160
	v_fmac_f32_e32 v61, v31, v161
	s_waitcnt lgkmcnt(1)
	v_fmac_f32_e32 v75, v31, v162
	v_fmac_f32_e32 v74, v31, v163
	v_fmac_f32_e32 v59, v31, v164
	v_fmac_f32_e32 v40, v31, v165
	s_waitcnt lgkmcnt(0)
	v_fmac_f32_e32 v71, v31, v166
	v_fmac_f32_e32 v69, v31, v167
	v_fmac_f32_e32 v3, v31, v168
	ds_read_b128 v[32:35], v84 offset:24576
	v_fmac_f32_e32 v1, v31, v169
	ds_read_b128 v[158:161], v84 offset:25600
	ds_read_b128 v[162:165], v84 offset:26624
	ds_read_b128 v[166:169], v84 offset:27648
	s_waitcnt lgkmcnt(3)
	v_fmac_f32_e32 v156, v28, v32
	v_fmac_f32_e32 v155, v28, v33
	s_waitcnt lgkmcnt(2)
	v_fmac_f32_e32 v77, v28, v158
	v_fmac_f32_e32 v76, v28, v159
	v_fmac_f32_e32 v63, v28, v160
	v_fmac_f32_e32 v61, v28, v161
	s_waitcnt lgkmcnt(1)
	v_fmac_f32_e32 v75, v28, v162
	v_fmac_f32_e32 v74, v28, v163
	v_fmac_f32_e32 v59, v28, v164
	v_fmac_f32_e32 v40, v28, v165
	s_waitcnt lgkmcnt(0)
	v_fmac_f32_e32 v71, v28, v166
	v_fmac_f32_e32 v69, v28, v167
	v_fmac_f32_e32 v3, v28, v168
	ds_read_b128 v[30:33], v84 offset:28672
	v_fmac_f32_e32 v1, v28, v169
	ds_read_b128 v[158:161], v84 offset:29696
	ds_read_b128 v[162:165], v84 offset:30720
	ds_read_b128 v[166:169], v84 offset:31744
	v_fmac_f32_e32 v67, v28, v34
	v_fmac_f32_e32 v65, v28, v35
	s_waitcnt lgkmcnt(3)
	v_fmac_f32_e32 v156, v29, v30
	s_waitcnt lgkmcnt(1)
	v_fmac_f32_e32 v59, v29, v164
	v_fmac_f32_e32 v40, v29, v165
	s_waitcnt lgkmcnt(0)
	v_fmac_f32_e32 v3, v29, v168
	v_fmac_f32_e32 v1, v29, v169
	v_fmac_f32_e32 v155, v29, v31
	v_fmac_f32_e32 v67, v29, v32
	v_fmac_f32_e32 v65, v29, v33
	v_fmac_f32_e32 v77, v29, v158
	v_fmac_f32_e32 v76, v29, v159
	v_fmac_f32_e32 v63, v29, v160
	v_fmac_f32_e32 v61, v29, v161
	v_fmac_f32_e32 v75, v29, v162
	v_fmac_f32_e32 v74, v29, v163
	v_fmac_f32_e32 v71, v29, v166
	v_fmac_f32_e32 v69, v29, v167
	ds_read_b128 v[28:31], v84 offset:32768
	ds_read_b128 v[32:35], v84 offset:33792
	ds_read_b128 v[158:161], v84 offset:34816
	ds_read_b128 v[162:165], v84 offset:35840
	s_waitcnt lgkmcnt(3)
	v_fmac_f32_e32 v156, v26, v28
	v_fmac_f32_e32 v155, v26, v29
	v_fmac_f32_e32 v67, v26, v30
	v_fmac_f32_e32 v65, v26, v31
	s_waitcnt lgkmcnt(2)
	v_fmac_f32_e32 v77, v26, v32
	v_fmac_f32_e32 v76, v26, v33
	v_fmac_f32_e32 v63, v26, v34
	v_fmac_f32_e32 v61, v26, v35
	s_waitcnt lgkmcnt(1)
	v_fmac_f32_e32 v75, v26, v158
	v_fmac_f32_e32 v74, v26, v159
	v_fmac_f32_e32 v59, v26, v160
	v_fmac_f32_e32 v40, v26, v161
	s_waitcnt lgkmcnt(0)
	v_fmac_f32_e32 v71, v26, v162
	v_fmac_f32_e32 v69, v26, v163
	v_fmac_f32_e32 v3, v26, v164
	ds_read_b128 v[28:31], v84 offset:36864
	v_fmac_f32_e32 v1, v26, v165
	ds_read_b128 v[32:35], v84 offset:37888
	ds_read_b128 v[158:161], v84 offset:38912
	ds_read_b128 v[162:165], v84 offset:39936
	s_waitcnt lgkmcnt(3)
	v_fmac_f32_e32 v156, v27, v28
	v_fmac_f32_e32 v155, v27, v29
	v_fmac_f32_e32 v67, v27, v30
	v_fmac_f32_e32 v65, v27, v31
	s_waitcnt lgkmcnt(2)
	v_fmac_f32_e32 v77, v27, v32
	v_fmac_f32_e32 v76, v27, v33
	v_fmac_f32_e32 v63, v27, v34
	v_fmac_f32_e32 v61, v27, v35
	s_waitcnt lgkmcnt(1)
	v_fmac_f32_e32 v75, v27, v158
	v_fmac_f32_e32 v74, v27, v159
	v_fmac_f32_e32 v59, v27, v160
	v_fmac_f32_e32 v40, v27, v161
	s_waitcnt lgkmcnt(0)
	v_fmac_f32_e32 v71, v27, v162
	v_fmac_f32_e32 v69, v27, v163
	v_fmac_f32_e32 v3, v27, v164
	ds_read_b128 v[28:31], v84 offset:40960
	v_fmac_f32_e32 v1, v27, v165
	ds_read_b128 v[32:35], v84 offset:41984
	ds_read_b128 v[158:161], v84 offset:43008
	ds_read_b128 v[162:165], v84 offset:44032
	s_waitcnt lgkmcnt(3)
	v_fmac_f32_e32 v156, v24, v28
	v_fmac_f32_e32 v155, v24, v29
	v_fmac_f32_e32 v67, v24, v30
	v_fmac_f32_e32 v65, v24, v31
	s_waitcnt lgkmcnt(2)
	v_fmac_f32_e32 v77, v24, v32
	v_fmac_f32_e32 v76, v24, v33
	s_waitcnt lgkmcnt(1)
	v_fmac_f32_e32 v75, v24, v158
	v_fmac_f32_e32 v74, v24, v159
	v_fmac_f32_e32 v59, v24, v160
	v_fmac_f32_e32 v40, v24, v161
	s_waitcnt lgkmcnt(0)
	v_fmac_f32_e32 v71, v24, v162
	v_fmac_f32_e32 v69, v24, v163
	v_fmac_f32_e32 v3, v24, v164
	ds_read_b128 v[26:29], v84 offset:45056
	v_fmac_f32_e32 v1, v24, v165
	ds_read_b128 v[30:33], v84 offset:46080
	ds_read_b128 v[158:161], v84 offset:47104
	ds_read_b128 v[162:165], v84 offset:48128
	v_fmac_f32_e32 v63, v24, v34
	v_fmac_f32_e32 v61, v24, v35
	s_waitcnt lgkmcnt(3)
	v_fmac_f32_e32 v156, v25, v26
	s_waitcnt lgkmcnt(1)
	v_fmac_f32_e32 v59, v25, v160
	v_fmac_f32_e32 v40, v25, v161
	s_waitcnt lgkmcnt(0)
	v_fmac_f32_e32 v3, v25, v164
	v_fmac_f32_e32 v1, v25, v165
	v_fmac_f32_e32 v155, v25, v27
	v_fmac_f32_e32 v67, v25, v28
	v_fmac_f32_e32 v65, v25, v29
	v_fmac_f32_e32 v77, v25, v30
	v_fmac_f32_e32 v76, v25, v31
	v_fmac_f32_e32 v63, v25, v32
	v_fmac_f32_e32 v61, v25, v33
	v_fmac_f32_e32 v75, v25, v158
	v_fmac_f32_e32 v74, v25, v159
	v_fmac_f32_e32 v71, v25, v162
	v_fmac_f32_e32 v69, v25, v163
	ds_read_b128 v[24:27], v84 offset:49152
	ds_read_b128 v[28:31], v84 offset:50176
	ds_read_b128 v[32:35], v84 offset:51200
	ds_read_b128 v[158:161], v84 offset:52224
	s_waitcnt lgkmcnt(3)
	v_fmac_f32_e32 v156, v22, v24
	v_fmac_f32_e32 v155, v22, v25
	v_fmac_f32_e32 v67, v22, v26
	v_fmac_f32_e32 v65, v22, v27
	s_waitcnt lgkmcnt(2)
	v_fmac_f32_e32 v77, v22, v28
	v_fmac_f32_e32 v76, v22, v29
	v_fmac_f32_e32 v63, v22, v30
	v_fmac_f32_e32 v61, v22, v31
	s_waitcnt lgkmcnt(1)
	v_fmac_f32_e32 v75, v22, v32
	v_fmac_f32_e32 v74, v22, v33
	v_fmac_f32_e32 v59, v22, v34
	v_fmac_f32_e32 v40, v22, v35
	s_waitcnt lgkmcnt(0)
; template <bool COMBINE, bool ROUTE, bool FINAL, bool OUT8 = false, bool DUMMY = false> ...
;     ...
;                 for (int j = 0; j < 8; ++j) {
; #pragma unroll
;                     for (int cc = 0; cc < 4; ++cc) {
;                         const float hv = xv[j][cc];
;                         const f32x4 w0 = WT[((j * 4 + cc) * 4 + 0) * 64 + lane], w1 = WT[((j * 4 + cc) * 4 + 1) * 64 + lane], w2 = WT[((j * 4 + cc) * 4 + 2) * 64 + lane], w3 = WT[((j * 4 + cc) * 4 + 3) * 64 + lane];
;                         lg[0] += hv * w0.x; lg[1] += hv * w0.y; lg[2] += hv * w0.z; lg[3] += hv * w0.w;
;                         lg[4] += hv * w1.x; lg[5] += hv * w1.y; lg[6] += hv * w1.z; lg[7] += hv * w1.w;
;                         lg[8] += hv * w2.x; lg[9] += hv * w2.y; lg[10] += hv * w2.z; lg[11] += hv * w2.w;
;                         lg[12] += hv * w3.x; lg[13] += hv * w3.y; lg[14] += hv * w3.z; lg[15] += hv * w3.w;
;                     }
	v_fmac_f32_e32 v71, v22, v158
	v_fmac_f32_e32 v69, v22, v159
	v_fmac_f32_e32 v3, v22, v160
	ds_read_b128 v[24:27], v84 offset:53248
	v_fmac_f32_e32 v1, v22, v161
	ds_read_b128 v[28:31], v84 offset:54272
	ds_read_b128 v[32:35], v84 offset:55296
	ds_read_b128 v[158:161], v84 offset:56320
	s_waitcnt lgkmcnt(3)
	v_fmac_f32_e32 v156, v23, v24
	v_fmac_f32_e32 v155, v23, v25
	v_fmac_f32_e32 v67, v23, v26
	v_fmac_f32_e32 v65, v23, v27
	s_waitcnt lgkmcnt(2)
	v_fmac_f32_e32 v77, v23, v28
	v_fmac_f32_e32 v76, v23, v29
	v_fmac_f32_e32 v63, v23, v30
	v_fmac_f32_e32 v61, v23, v31
	s_waitcnt lgkmcnt(1)
	v_fmac_f32_e32 v75, v23, v32
	v_fmac_f32_e32 v74, v23, v33
	v_fmac_f32_e32 v59, v23, v34
	v_fmac_f32_e32 v40, v23, v35
	s_waitcnt lgkmcnt(0)
	v_fmac_f32_e32 v71, v23, v158
	v_fmac_f32_e32 v69, v23, v159
	v_fmac_f32_e32 v3, v23, v160
	ds_read_b128 v[24:27], v84 offset:57344
	v_fmac_f32_e32 v1, v23, v161
	ds_read_b128 v[28:31], v84 offset:58368
	ds_read_b128 v[32:35], v84 offset:59392
	ds_read_b128 v[158:161], v84 offset:60416
	s_waitcnt lgkmcnt(3)
	v_fmac_f32_e32 v156, v20, v24
	v_fmac_f32_e32 v155, v20, v25
	v_fmac_f32_e32 v67, v20, v26
	v_fmac_f32_e32 v65, v20, v27
	s_waitcnt lgkmcnt(2)
	v_fmac_f32_e32 v77, v20, v28
	v_fmac_f32_e32 v76, v20, v29
	v_fmac_f32_e32 v63, v20, v30
	v_fmac_f32_e32 v61, v20, v31
	s_waitcnt lgkmcnt(1)
	v_fmac_f32_e32 v75, v20, v32
	v_fmac_f32_e32 v74, v20, v33
	s_waitcnt lgkmcnt(0)
	v_fmac_f32_e32 v71, v20, v158
	v_fmac_f32_e32 v69, v20, v159
	v_fmac_f32_e32 v3, v20, v160
	ds_read_b128 v[22:25], v84 offset:61440
	v_fmac_f32_e32 v1, v20, v161
	ds_read_b128 v[26:29], v84 offset:62464
	ds_read_b128 v[30:33], v84 offset:63488
	ds_read_b128 v[158:161], v84 offset:64512
	v_fmac_f32_e32 v59, v20, v34
	v_fmac_f32_e32 v40, v20, v35
	s_waitcnt lgkmcnt(3)
	v_fmac_f32_e32 v156, v21, v22
	s_waitcnt lgkmcnt(1)
	v_fmac_f32_e32 v59, v21, v32
	v_fmac_f32_e32 v40, v21, v33
	s_waitcnt lgkmcnt(0)
	v_fmac_f32_e32 v3, v21, v160
	v_fmac_f32_e32 v1, v21, v161
	v_fmac_f32_e32 v155, v21, v23
	v_fmac_f32_e32 v67, v21, v24
	v_fmac_f32_e32 v65, v21, v25
	v_fmac_f32_e32 v77, v21, v26
	v_fmac_f32_e32 v76, v21, v27
	v_fmac_f32_e32 v63, v21, v28
	v_fmac_f32_e32 v61, v21, v29
	v_fmac_f32_e32 v75, v21, v30
	v_fmac_f32_e32 v74, v21, v31
	v_fmac_f32_e32 v71, v21, v158
	v_fmac_f32_e32 v69, v21, v159
	ds_read_b128 v[20:23], v86
	ds_read_b128 v[24:27], v87
	ds_read_b128 v[28:31], v88
	ds_read_b128 v[32:35], v89
	s_waitcnt lgkmcnt(3)
	v_fmac_f32_e32 v156, v18, v20
	v_fmac_f32_e32 v155, v18, v21
	v_fmac_f32_e32 v67, v18, v22
	v_fmac_f32_e32 v65, v18, v23
	s_waitcnt lgkmcnt(2)
	v_fmac_f32_e32 v77, v18, v24
	v_fmac_f32_e32 v76, v18, v25
	v_fmac_f32_e32 v63, v18, v26
	v_fmac_f32_e32 v61, v18, v27
	s_waitcnt lgkmcnt(1)
	v_fmac_f32_e32 v75, v18, v28
	v_fmac_f32_e32 v74, v18, v29
	v_fmac_f32_e32 v59, v18, v30
	v_fmac_f32_e32 v40, v18, v31
	s_waitcnt lgkmcnt(0)
	v_fmac_f32_e32 v71, v18, v32
	v_fmac_f32_e32 v69, v18, v33
	v_fmac_f32_e32 v3, v18, v34
	ds_read_b128 v[20:23], v90
	v_fmac_f32_e32 v1, v18, v35
	ds_read_b128 v[24:27], v91
	ds_read_b128 v[28:31], v92
	ds_read_b128 v[32:35], v93
	s_waitcnt lgkmcnt(3)
	v_fmac_f32_e32 v156, v19, v20
	v_fmac_f32_e32 v155, v19, v21
	v_fmac_f32_e32 v67, v19, v22
	v_fmac_f32_e32 v65, v19, v23
	s_waitcnt lgkmcnt(2)
	v_fmac_f32_e32 v77, v19, v24
	v_fmac_f32_e32 v76, v19, v25
	v_fmac_f32_e32 v63, v19, v26
	v_fmac_f32_e32 v61, v19, v27
	s_waitcnt lgkmcnt(1)
	v_fmac_f32_e32 v75, v19, v28
	v_fmac_f32_e32 v74, v19, v29
	v_fmac_f32_e32 v59, v19, v30
	v_fmac_f32_e32 v40, v19, v31
	s_waitcnt lgkmcnt(0)
	v_fmac_f32_e32 v71, v19, v32
	v_fmac_f32_e32 v69, v19, v33
	v_fmac_f32_e32 v3, v19, v34
	ds_read_b128 v[20:23], v94
	v_fmac_f32_e32 v1, v19, v35
	ds_read_b128 v[24:27], v95
	ds_read_b128 v[28:31], v96
	ds_read_b128 v[32:35], v97
	s_waitcnt lgkmcnt(3)
	v_fmac_f32_e32 v156, v16, v20
	v_fmac_f32_e32 v155, v16, v21
	v_fmac_f32_e32 v67, v16, v22
	v_fmac_f32_e32 v65, v16, v23
	s_waitcnt lgkmcnt(2)
	v_fmac_f32_e32 v77, v16, v24
	v_fmac_f32_e32 v76, v16, v25
	v_fmac_f32_e32 v63, v16, v26
	v_fmac_f32_e32 v61, v16, v27
	s_waitcnt lgkmcnt(1)
	v_fmac_f32_e32 v75, v16, v28
	v_fmac_f32_e32 v74, v16, v29
	v_fmac_f32_e32 v59, v16, v30
	v_fmac_f32_e32 v40, v16, v31
	s_waitcnt lgkmcnt(0)
	v_fmac_f32_e32 v71, v16, v32
	v_fmac_f32_e32 v69, v16, v33
	ds_read_b128 v[18:21], v98
	ds_read_b128 v[22:25], v99
	ds_read_b128 v[26:29], v100
	ds_read_b128 v[30:33], v101
	v_fmac_f32_e32 v3, v16, v34
	v_fmac_f32_e32 v1, v16, v35
	s_waitcnt lgkmcnt(2)
	v_fmac_f32_e32 v77, v17, v22
	s_waitcnt lgkmcnt(1)
	v_fmac_f32_e32 v59, v17, v28
	v_fmac_f32_e32 v40, v17, v29
	s_waitcnt lgkmcnt(0)
	v_fmac_f32_e32 v3, v17, v32
	v_fmac_f32_e32 v1, v17, v33
	v_fmac_f32_e32 v156, v17, v18
	v_fmac_f32_e32 v155, v17, v19
	v_fmac_f32_e32 v67, v17, v20
	v_fmac_f32_e32 v65, v17, v21
	v_fmac_f32_e32 v76, v17, v23
	v_fmac_f32_e32 v63, v17, v24
	v_fmac_f32_e32 v61, v17, v25
	v_fmac_f32_e32 v75, v17, v26
	v_fmac_f32_e32 v74, v17, v27
	v_fmac_f32_e32 v71, v17, v30
	v_fmac_f32_e32 v69, v17, v31
	ds_read_b128 v[16:19], v102
	ds_read_b128 v[20:23], v103
	ds_read_b128 v[24:27], v104
	ds_read_b128 v[28:31], v105
	s_waitcnt lgkmcnt(3)
	v_fmac_f32_e32 v156, v14, v16
	v_fmac_f32_e32 v155, v14, v17
	v_fmac_f32_e32 v67, v14, v18
	v_fmac_f32_e32 v65, v14, v19
	s_waitcnt lgkmcnt(2)
	v_fmac_f32_e32 v77, v14, v20
	v_fmac_f32_e32 v76, v14, v21
	v_fmac_f32_e32 v63, v14, v22
	v_fmac_f32_e32 v61, v14, v23
	s_waitcnt lgkmcnt(1)
	v_fmac_f32_e32 v75, v14, v24
	v_fmac_f32_e32 v74, v14, v25
	v_fmac_f32_e32 v59, v14, v26
	v_fmac_f32_e32 v40, v14, v27
	s_waitcnt lgkmcnt(0)
; template <bool COMBINE, bool ROUTE, bool FINAL, bool OUT8 = false, bool DUMMY = false> ...
;     ...
;                 for (int j = 0; j < 8; ++j) {
; #pragma unroll
;                     for (int cc = 0; cc < 4; ++cc) {
;                         const float hv = xv[j][cc];
;                         const f32x4 w0 = WT[((j * 4 + cc) * 4 + 0) * 64 + lane], w1 = WT[((j * 4 + cc) * 4 + 1) * 64 + lane], w2 = WT[((j * 4 + cc) * 4 + 2) * 64 + lane], w3 = WT[((j * 4 + cc) * 4 + 3) * 64 + lane];
;                         lg[0] += hv * w0.x; lg[1] += hv * w0.y; lg[2] += hv * w0.z; lg[3] += hv * w0.w;
;                         lg[4] += hv * w1.x; lg[5] += hv * w1.y; lg[6] += hv * w1.z; lg[7] += hv * w1.w;
;                         lg[8] += hv * w2.x; lg[9] += hv * w2.y; lg[10] += hv * w2.z; lg[11] += hv * w2.w;
;                         lg[12] += hv * w3.x; lg[13] += hv * w3.y; lg[14] += hv * w3.z; lg[15] += hv * w3.w;
;                     }
	v_fmac_f32_e32 v71, v14, v28
	v_fmac_f32_e32 v69, v14, v29
	v_fmac_f32_e32 v3, v14, v30
	ds_read_b128 v[16:19], v106
	v_fmac_f32_e32 v1, v14, v31
	ds_read_b128 v[20:23], v107
	ds_read_b128 v[24:27], v108
	ds_read_b128 v[28:31], v109
	s_waitcnt lgkmcnt(3)
	v_fmac_f32_e32 v156, v15, v16
	v_fmac_f32_e32 v155, v15, v17
	v_fmac_f32_e32 v67, v15, v18
	v_fmac_f32_e32 v65, v15, v19
	s_waitcnt lgkmcnt(2)
	v_fmac_f32_e32 v77, v15, v20
	v_fmac_f32_e32 v76, v15, v21
	v_fmac_f32_e32 v63, v15, v22
	v_fmac_f32_e32 v61, v15, v23
	s_waitcnt lgkmcnt(1)
	v_fmac_f32_e32 v75, v15, v24
	v_fmac_f32_e32 v74, v15, v25
	v_fmac_f32_e32 v59, v15, v26
	v_fmac_f32_e32 v40, v15, v27
	s_waitcnt lgkmcnt(0)
	v_fmac_f32_e32 v71, v15, v28
	v_fmac_f32_e32 v69, v15, v29
	v_fmac_f32_e32 v3, v15, v30
	ds_read_b128 v[16:19], v110
	v_fmac_f32_e32 v1, v15, v31
	ds_read_b128 v[20:23], v111
	ds_read_b128 v[24:27], v112
	ds_read_b128 v[28:31], v113
	s_waitcnt lgkmcnt(3)
	v_fmac_f32_e32 v156, v12, v16
	v_fmac_f32_e32 v155, v12, v17
	v_fmac_f32_e32 v67, v12, v18
	v_fmac_f32_e32 v65, v12, v19
	s_waitcnt lgkmcnt(2)
	v_fmac_f32_e32 v77, v12, v20
	v_fmac_f32_e32 v76, v12, v21
	v_fmac_f32_e32 v63, v12, v22
	v_fmac_f32_e32 v61, v12, v23
	s_waitcnt lgkmcnt(1)
	v_fmac_f32_e32 v75, v12, v24
	v_fmac_f32_e32 v74, v12, v25
	v_fmac_f32_e32 v59, v12, v26
	v_fmac_f32_e32 v40, v12, v27
	s_waitcnt lgkmcnt(0)
	v_fmac_f32_e32 v71, v12, v28
	v_fmac_f32_e32 v69, v12, v29
	ds_read_b128 v[14:17], v114
	ds_read_b128 v[18:21], v115
	ds_read_b128 v[22:25], v116
	ds_read_b128 v[26:29], v117
	v_fmac_f32_e32 v3, v12, v30
	v_fmac_f32_e32 v1, v12, v31
	s_waitcnt lgkmcnt(2)
	v_fmac_f32_e32 v77, v13, v18
	s_waitcnt lgkmcnt(1)
	v_fmac_f32_e32 v59, v13, v24
	v_fmac_f32_e32 v40, v13, v25
	s_waitcnt lgkmcnt(0)
	v_fmac_f32_e32 v3, v13, v28
	v_fmac_f32_e32 v1, v13, v29
	v_fmac_f32_e32 v156, v13, v14
	v_fmac_f32_e32 v155, v13, v15
	v_fmac_f32_e32 v67, v13, v16
	v_fmac_f32_e32 v65, v13, v17
	v_fmac_f32_e32 v76, v13, v19
	v_fmac_f32_e32 v63, v13, v20
	v_fmac_f32_e32 v61, v13, v21
	v_fmac_f32_e32 v75, v13, v22
	v_fmac_f32_e32 v74, v13, v23
	v_fmac_f32_e32 v71, v13, v26
	v_fmac_f32_e32 v69, v13, v27
	ds_read_b128 v[12:15], v118
	ds_read_b128 v[16:19], v119
	ds_read_b128 v[20:23], v120
	ds_read_b128 v[24:27], v121
	s_waitcnt lgkmcnt(3)
	v_fmac_f32_e32 v156, v10, v12
	v_fmac_f32_e32 v155, v10, v13
	v_fmac_f32_e32 v67, v10, v14
	v_fmac_f32_e32 v65, v10, v15
	s_waitcnt lgkmcnt(2)
	v_fmac_f32_e32 v77, v10, v16
	v_fmac_f32_e32 v76, v10, v17
	v_fmac_f32_e32 v63, v10, v18
	v_fmac_f32_e32 v61, v10, v19
	s_waitcnt lgkmcnt(1)
	v_fmac_f32_e32 v75, v10, v20
	v_fmac_f32_e32 v74, v10, v21
	v_fmac_f32_e32 v59, v10, v22
	v_fmac_f32_e32 v40, v10, v23
	s_waitcnt lgkmcnt(0)
	v_fmac_f32_e32 v71, v10, v24
	v_fmac_f32_e32 v69, v10, v25
	v_fmac_f32_e32 v3, v10, v26
	ds_read_b128 v[12:15], v122
	v_fmac_f32_e32 v1, v10, v27
	ds_read_b128 v[16:19], v123
	ds_read_b128 v[20:23], v124
	ds_read_b128 v[24:27], v125
	s_waitcnt lgkmcnt(3)
	v_fmac_f32_e32 v156, v11, v12
	v_fmac_f32_e32 v155, v11, v13
	v_fmac_f32_e32 v67, v11, v14
	v_fmac_f32_e32 v65, v11, v15
	s_waitcnt lgkmcnt(2)
	v_fmac_f32_e32 v77, v11, v16
	v_fmac_f32_e32 v76, v11, v17
	v_fmac_f32_e32 v63, v11, v18
	v_fmac_f32_e32 v61, v11, v19
	s_waitcnt lgkmcnt(1)
	v_fmac_f32_e32 v75, v11, v20
	v_fmac_f32_e32 v74, v11, v21
	v_fmac_f32_e32 v59, v11, v22
	v_fmac_f32_e32 v40, v11, v23
	s_waitcnt lgkmcnt(0)
	v_fmac_f32_e32 v71, v11, v24
	v_fmac_f32_e32 v69, v11, v25
	v_fmac_f32_e32 v3, v11, v26
	ds_read_b128 v[12:15], v126
	v_fmac_f32_e32 v1, v11, v27
	ds_read_b128 v[16:19], v127
	ds_read_b128 v[20:23], v128
	ds_read_b128 v[24:27], v129
	s_waitcnt lgkmcnt(3)
	v_fmac_f32_e32 v156, v8, v12
	v_fmac_f32_e32 v155, v8, v13
	v_fmac_f32_e32 v67, v8, v14
	v_fmac_f32_e32 v65, v8, v15
	s_waitcnt lgkmcnt(2)
	v_fmac_f32_e32 v77, v8, v16
	v_fmac_f32_e32 v76, v8, v17
	v_fmac_f32_e32 v63, v8, v18
	v_fmac_f32_e32 v61, v8, v19
	s_waitcnt lgkmcnt(1)
	v_fmac_f32_e32 v75, v8, v20
	v_fmac_f32_e32 v74, v8, v21
	v_fmac_f32_e32 v59, v8, v22
	v_fmac_f32_e32 v40, v8, v23
	s_waitcnt lgkmcnt(0)
	v_fmac_f32_e32 v71, v8, v24
	v_fmac_f32_e32 v69, v8, v25
	ds_read_b128 v[10:13], v130
	ds_read_b128 v[14:17], v131
	ds_read_b128 v[18:21], v132
	ds_read_b128 v[22:25], v133
	v_fmac_f32_e32 v3, v8, v26
	v_fmac_f32_e32 v1, v8, v27
	s_waitcnt lgkmcnt(2)
	v_fmac_f32_e32 v77, v9, v14
	s_waitcnt lgkmcnt(1)
	v_fmac_f32_e32 v59, v9, v20
	v_fmac_f32_e32 v40, v9, v21
	s_waitcnt lgkmcnt(0)
	v_fmac_f32_e32 v3, v9, v24
	v_fmac_f32_e32 v1, v9, v25
	v_fmac_f32_e32 v156, v9, v10
	v_fmac_f32_e32 v155, v9, v11
	v_fmac_f32_e32 v67, v9, v12
	v_fmac_f32_e32 v65, v9, v13
	v_fmac_f32_e32 v76, v9, v15
	v_fmac_f32_e32 v63, v9, v16
	v_fmac_f32_e32 v61, v9, v17
	v_fmac_f32_e32 v75, v9, v18
	v_fmac_f32_e32 v74, v9, v19
	v_fmac_f32_e32 v71, v9, v22
	v_fmac_f32_e32 v69, v9, v23
	ds_read_b128 v[8:11], v134
	ds_read_b128 v[12:15], v135
	ds_read_b128 v[16:19], v136
	ds_read_b128 v[20:23], v137
	s_waitcnt lgkmcnt(3)
	v_fmac_f32_e32 v65, v6, v11
	v_fmac_f32_e32 v67, v6, v10
	v_mov_b32_e32 v10, v8
	s_waitcnt lgkmcnt(0)
	v_fmac_f32_e32 v3, v6, v22
	v_fmac_f32_e32 v1, v6, v23
	ds_read_b128 v[22:25], v138
	ds_read_b128 v[26:29], v139
	ds_read_b128 v[30:33], v140
	ds_read_b128 v[158:161], v141
	v_fmac_f32_e32 v63, v6, v14
	s_waitcnt lgkmcnt(3)
	v_mov_b32_e32 v11, v22
	v_mov_b32_e32 v22, v9
	v_pk_mul_f32 v[8:9], v[6:7], v[22:23]
	v_pk_mul_f32 v[10:11], v[6:7], v[10:11]
	v_add_f32_e32 v8, v155, v8
	v_add_f32_e32 v155, v8, v9
	v_mov_b32_e32 v8, v12
	s_waitcnt lgkmcnt(2)
; template <bool COMBINE, bool ROUTE, bool FINAL, bool OUT8 = false, bool DUMMY = false> ...
;     ...
;                         lg[0] += hv * w0.x; lg[1] += hv * w0.y; lg[2] += hv * w0.z; lg[3] += hv * w0.w;
;                         lg[4] += hv * w1.x; lg[5] += hv * w1.y; lg[6] += hv * w1.z; lg[7] += hv * w1.w;
;                         lg[8] += hv * w2.x; lg[9] += hv * w2.y; lg[10] += hv * w2.z; lg[11] += hv * w2.w;
;                         lg[12] += hv * w3.x; lg[13] += hv * w3.y; lg[14] += hv * w3.z; lg[15] += hv * w3.w;
;                     }
;                     __builtin_amdgcn_sched_barrier(0);
;                 }
;                 float sc_[16], sel[16];
; #pragma unroll
;                 for (int e = 0; e < 16; ++e) { lg[e] = wave_sum(lg[e]); sc_[e] = 1.f / (1.f + expf(-lg[e])); sel[e] = sc_[e] + rb[e]; }
	v_mov_b32_e32 v9, v26
	v_pk_mul_f32 v[8:9], v[6:7], v[8:9]
	v_mov_b32_e32 v26, v13
	v_add_f32_e32 v8, v77, v8
	v_add_f32_e32 v77, v8, v9
	v_pk_mul_f32 v[8:9], v[6:7], v[26:27]
	v_add_f32_e32 v0, v156, v10
	v_add_f32_e32 v8, v76, v8
	v_add_f32_e32 v76, v8, v9
	v_mov_b32_e32 v8, v16
	s_waitcnt lgkmcnt(1)
	v_mov_b32_e32 v9, v30
	v_pk_mul_f32 v[8:9], v[6:7], v[8:9]
	v_mov_b32_e32 v30, v17
	v_add_f32_e32 v8, v75, v8
	v_add_f32_e32 v156, v8, v9
	v_pk_mul_f32 v[8:9], v[6:7], v[30:31]
	v_fmac_f32_e32 v61, v6, v15
	v_add_f32_e32 v8, v74, v8
	v_add_f32_e32 v157, v8, v9
	v_mov_b32_e32 v8, v20
	s_waitcnt lgkmcnt(0)
	v_mov_b32_e32 v9, v158
	v_pk_mul_f32 v[8:9], v[6:7], v[8:9]
	v_mov_b32_e32 v158, v21
	v_add_f32_e32 v8, v71, v8
	v_add_f32_e32 v71, v8, v9
	v_pk_mul_f32 v[8:9], v[6:7], v[158:159]
	v_fmac_f32_e32 v59, v6, v18
	v_fmac_f32_e32 v40, v6, v19
	v_add_f32_e32 v6, v69, v8
	v_add_f32_e32 v0, v0, v11
	v_fmac_f32_e32 v67, v7, v24
	v_fmac_f32_e32 v65, v7, v25
	v_fmac_f32_e32 v63, v7, v28
	v_fmac_f32_e32 v61, v7, v29
	v_fmac_f32_e32 v59, v7, v32
	v_fmac_f32_e32 v40, v7, v33
	v_add_f32_e32 v69, v6, v9
	v_fmac_f32_e32 v3, v7, v160
	v_fmac_f32_e32 v1, v7, v161
	ds_read_b128 v[6:9], v142
	ds_read_b128 v[10:13], v143
	ds_read_b128 v[14:17], v144
	ds_read_b128 v[18:21], v145
	ds_read_b128 v[22:25], v146
	ds_read_b128 v[26:29], v147
	ds_read_b128 v[30:33], v148
	ds_read_b128 v[72:75], v149
	s_waitcnt lgkmcnt(7)
	v_mov_b32_e32 v34, v6
	s_waitcnt lgkmcnt(3)
	v_mov_b32_e32 v35, v22
	v_mov_b32_e32 v22, v7
	v_pk_mul_f32 v[6:7], v[4:5], v[22:23]
	v_pk_mul_f32 v[34:35], v[4:5], v[34:35]
	v_add_f32_e32 v6, v155, v6
	v_add_f32_e32 v0, v0, v34
	v_add_f32_e32 v34, v6, v7
	v_mov_b32_e32 v6, v8
	v_mov_b32_e32 v7, v24
	v_pk_mul_f32 v[6:7], v[4:5], v[6:7]
	v_mov_b32_e32 v24, v9
	v_add_f32_e32 v6, v67, v6
	v_add_f32_e32 v8, v6, v7
	v_pk_mul_f32 v[6:7], v[4:5], v[24:25]
	v_add_f32_e32 v0, v0, v35
	v_add_f32_e32 v6, v65, v6
	v_add_f32_e32 v9, v6, v7
	v_mov_b32_e32 v6, v10
	s_waitcnt lgkmcnt(2)
	v_mov_b32_e32 v7, v26
	v_pk_mul_f32 v[6:7], v[4:5], v[6:7]
	v_mov_b32_e32 v26, v11
	v_add_f32_e32 v6, v77, v6
	v_add_f32_e32 v35, v6, v7
	v_pk_mul_f32 v[6:7], v[4:5], v[26:27]
	s_nop 0
	v_add_f32_e32 v6, v76, v6
	v_add_f32_e32 v65, v6, v7
	v_mov_b32_e32 v6, v12
	v_mov_b32_e32 v7, v28
	v_pk_mul_f32 v[6:7], v[4:5], v[6:7]
	v_mov_b32_e32 v28, v13
	v_add_f32_e32 v6, v63, v6
	v_add_f32_e32 v63, v6, v7
	v_pk_mul_f32 v[6:7], v[4:5], v[28:29]
	s_nop 0
	v_add_f32_e32 v6, v61, v6
	v_add_f32_e32 v61, v6, v7
	v_mov_b32_e32 v6, v14
	s_waitcnt lgkmcnt(1)
	v_mov_b32_e32 v7, v30
	v_pk_mul_f32 v[6:7], v[4:5], v[6:7]
	v_mov_b32_e32 v30, v15
	v_add_f32_e32 v6, v156, v6
	v_add_f32_e32 v27, v6, v7
	v_pk_mul_f32 v[6:7], v[4:5], v[30:31]
	s_nop 0
	v_add_f32_e32 v6, v157, v6
	v_add_f32_e32 v26, v6, v7
	v_mov_b32_e32 v6, v16
	v_mov_b32_e32 v7, v32
	v_pk_mul_f32 v[6:7], v[4:5], v[6:7]
	v_mov_b32_e32 v32, v17
	v_add_f32_e32 v6, v59, v6
	v_add_f32_e32 v25, v6, v7
	v_pk_mul_f32 v[6:7], v[4:5], v[32:33]
	s_nop 0
	v_add_f32_e32 v6, v40, v6
	v_add_f32_e32 v23, v6, v7
	v_mov_b32_e32 v6, v18
	s_waitcnt lgkmcnt(0)
	v_mov_b32_e32 v7, v72
	v_pk_mul_f32 v[6:7], v[4:5], v[6:7]
	v_mov_b32_e32 v72, v19
	v_add_f32_e32 v6, v71, v6
	v_add_f32_e32 v24, v6, v7
	v_pk_mul_f32 v[6:7], v[4:5], v[72:73]
	s_nop 0
	v_add_f32_e32 v6, v69, v6
	v_add_f32_e32 v22, v6, v7
	v_mov_b32_e32 v6, v20
	v_mov_b32_e32 v7, v74
	v_mov_b32_e32 v74, v21
	v_pk_mul_f32 v[6:7], v[4:5], v[6:7]
	v_pk_mul_f32 v[4:5], v[4:5], v[74:75]
	v_add_f32_e32 v3, v3, v6
	v_add_f32_e32 v1, v1, v4
	v_add_f32_e32 v3, v3, v7
	v_add_f32_e32 v1, v1, v5
	s_waitcnt lgkmcnt(0)
	ds_bpermute_b32 v160, v78, v0
	ds_bpermute_b32 v161, v78, v34
	ds_bpermute_b32 v162, v78, v8
	ds_bpermute_b32 v163, v78, v9
	ds_bpermute_b32 v164, v78, v35
	ds_bpermute_b32 v165, v78, v65
	ds_bpermute_b32 v166, v78, v61
	ds_bpermute_b32 v167, v78, v63
	s_waitcnt lgkmcnt(7)
	v_add_f32_e32 v0, v0, v160
	s_waitcnt lgkmcnt(6)
	v_add_f32_e32 v34, v34, v161
	s_waitcnt lgkmcnt(5)
	v_add_f32_e32 v8, v8, v162
	s_waitcnt lgkmcnt(4)
	v_add_f32_e32 v9, v9, v163
	s_waitcnt lgkmcnt(3)
	v_add_f32_e32 v35, v35, v164
	s_waitcnt lgkmcnt(2)
	v_add_f32_e32 v65, v65, v165
	s_waitcnt lgkmcnt(1)
	v_add_f32_e32 v61, v61, v166
	s_waitcnt lgkmcnt(0)
	v_add_f32_e32 v63, v63, v167
	ds_bpermute_b32 v168, v78, v27
	ds_bpermute_b32 v169, v78, v26
	ds_bpermute_b32 v170, v78, v25
	ds_bpermute_b32 v171, v78, v24
	ds_bpermute_b32 v172, v78, v23
	ds_bpermute_b32 v173, v78, v3
	ds_bpermute_b32 v174, v78, v22
	ds_bpermute_b32 v175, v78, v1
	s_waitcnt lgkmcnt(7)
	v_add_f32_e32 v27, v27, v168
	s_waitcnt lgkmcnt(6)
	v_add_f32_e32 v26, v26, v169
	s_waitcnt lgkmcnt(5)
	v_add_f32_e32 v25, v25, v170
	s_waitcnt lgkmcnt(4)
	v_add_f32_e32 v24, v24, v171
	s_waitcnt lgkmcnt(3)
	v_add_f32_e32 v23, v23, v172
	s_waitcnt lgkmcnt(2)
	v_add_f32_e32 v3, v3, v173
	s_waitcnt lgkmcnt(1)
	v_add_f32_e32 v22, v22, v174
	s_waitcnt lgkmcnt(0)
	v_add_f32_e32 v1, v1, v175
	ds_bpermute_b32 v160, v79, v0
	ds_bpermute_b32 v161, v79, v34
	ds_bpermute_b32 v162, v79, v8
	ds_bpermute_b32 v163, v79, v9
	ds_bpermute_b32 v164, v79, v35
	ds_bpermute_b32 v165, v79, v65
	ds_bpermute_b32 v166, v79, v61
	ds_bpermute_b32 v167, v79, v63
	s_waitcnt lgkmcnt(7)
	v_add_f32_e32 v0, v0, v160
	s_waitcnt lgkmcnt(6)
	v_add_f32_e32 v34, v34, v161
	s_waitcnt lgkmcnt(5)
	v_add_f32_e32 v8, v8, v162
	s_waitcnt lgkmcnt(4)
	v_add_f32_e32 v9, v9, v163
	s_waitcnt lgkmcnt(3)
	v_add_f32_e32 v35, v35, v164
	s_waitcnt lgkmcnt(2)
	v_add_f32_e32 v65, v65, v165
	s_waitcnt lgkmcnt(1)
	v_add_f32_e32 v61, v61, v166
	s_waitcnt lgkmcnt(0)
; template <bool COMBINE, bool ROUTE, bool FINAL, bool OUT8 = false, bool DUMMY = false> ...
;     ...
;                 for (int e = 0; e < 16; ++e) { lg[e] = wave_sum(lg[e]); sc_[e] = 1.f / (1.f + expf(-lg[e])); sel[e] = sc_[e] + rb[e]; }
	v_add_f32_e32 v63, v63, v167
	ds_bpermute_b32 v168, v79, v27
	ds_bpermute_b32 v169, v79, v26
	ds_bpermute_b32 v170, v79, v25
	ds_bpermute_b32 v171, v79, v24
	ds_bpermute_b32 v172, v79, v23
	ds_bpermute_b32 v173, v79, v3
	ds_bpermute_b32 v174, v79, v22
	ds_bpermute_b32 v175, v79, v1
	s_waitcnt lgkmcnt(7)
	v_add_f32_e32 v27, v27, v168
	s_waitcnt lgkmcnt(6)
	v_add_f32_e32 v26, v26, v169
	s_waitcnt lgkmcnt(5)
	v_add_f32_e32 v25, v25, v170
	s_waitcnt lgkmcnt(4)
	v_add_f32_e32 v24, v24, v171
	s_waitcnt lgkmcnt(3)
	v_add_f32_e32 v23, v23, v172
	s_waitcnt lgkmcnt(2)
	v_add_f32_e32 v3, v3, v173
	s_waitcnt lgkmcnt(1)
	v_add_f32_e32 v22, v22, v174
	s_waitcnt lgkmcnt(0)
	v_add_f32_e32 v1, v1, v175
	ds_bpermute_b32 v160, v80, v0
	ds_bpermute_b32 v161, v80, v34
	ds_bpermute_b32 v162, v80, v8
	ds_bpermute_b32 v163, v80, v9
	ds_bpermute_b32 v164, v80, v35
	ds_bpermute_b32 v165, v80, v65
	ds_bpermute_b32 v166, v80, v61
	ds_bpermute_b32 v167, v80, v63
	s_waitcnt lgkmcnt(7)
	v_add_f32_e32 v0, v0, v160
	s_waitcnt lgkmcnt(6)
	v_add_f32_e32 v34, v34, v161
	s_waitcnt lgkmcnt(5)
	v_add_f32_e32 v8, v8, v162
	s_waitcnt lgkmcnt(4)
	v_add_f32_e32 v9, v9, v163
	s_waitcnt lgkmcnt(3)
	v_add_f32_e32 v35, v35, v164
	s_waitcnt lgkmcnt(2)
	v_add_f32_e32 v65, v65, v165
	s_waitcnt lgkmcnt(1)
	v_add_f32_e32 v61, v61, v166
	s_waitcnt lgkmcnt(0)
	v_add_f32_e32 v63, v63, v167
	ds_bpermute_b32 v168, v80, v27
	ds_bpermute_b32 v169, v80, v26
	ds_bpermute_b32 v170, v80, v25
	ds_bpermute_b32 v171, v80, v24
	ds_bpermute_b32 v172, v80, v23
	ds_bpermute_b32 v173, v80, v3
	ds_bpermute_b32 v174, v80, v22
	ds_bpermute_b32 v175, v80, v1
	s_waitcnt lgkmcnt(7)
	v_add_f32_e32 v27, v27, v168
	s_waitcnt lgkmcnt(6)
	v_add_f32_e32 v26, v26, v169
	s_waitcnt lgkmcnt(5)
	v_add_f32_e32 v25, v25, v170
	s_waitcnt lgkmcnt(4)
	v_add_f32_e32 v24, v24, v171
	s_waitcnt lgkmcnt(3)
	v_add_f32_e32 v23, v23, v172
	s_waitcnt lgkmcnt(2)
	v_add_f32_e32 v3, v3, v173
	s_waitcnt lgkmcnt(1)
	v_add_f32_e32 v22, v22, v174
	s_waitcnt lgkmcnt(0)
	v_add_f32_e32 v1, v1, v175
	ds_bpermute_b32 v160, v81, v0
	ds_bpermute_b32 v161, v81, v34
	ds_bpermute_b32 v162, v81, v8
	ds_bpermute_b32 v163, v81, v9
	ds_bpermute_b32 v164, v81, v35
	ds_bpermute_b32 v165, v81, v65
	ds_bpermute_b32 v166, v81, v61
	ds_bpermute_b32 v167, v81, v63
	s_waitcnt lgkmcnt(7)
	v_add_f32_e32 v0, v0, v160
	s_waitcnt lgkmcnt(6)
	v_add_f32_e32 v34, v34, v161
	s_waitcnt lgkmcnt(5)
	v_add_f32_e32 v8, v8, v162
	s_waitcnt lgkmcnt(4)
	v_add_f32_e32 v9, v9, v163
	s_waitcnt lgkmcnt(3)
	v_add_f32_e32 v35, v35, v164
	s_waitcnt lgkmcnt(2)
	v_add_f32_e32 v65, v65, v165
	s_waitcnt lgkmcnt(1)
	v_add_f32_e32 v61, v61, v166
	s_waitcnt lgkmcnt(0)
	v_add_f32_e32 v63, v63, v167
	ds_bpermute_b32 v168, v81, v27
	ds_bpermute_b32 v169, v81, v26
	ds_bpermute_b32 v170, v81, v25
	ds_bpermute_b32 v171, v81, v24
	ds_bpermute_b32 v172, v81, v23
	ds_bpermute_b32 v173, v81, v3
	ds_bpermute_b32 v174, v81, v22
	ds_bpermute_b32 v175, v81, v1
	s_waitcnt lgkmcnt(7)
	v_add_f32_e32 v27, v27, v168
	s_waitcnt lgkmcnt(6)
	v_add_f32_e32 v26, v26, v169
	s_waitcnt lgkmcnt(5)
	v_add_f32_e32 v25, v25, v170
	s_waitcnt lgkmcnt(4)
	v_add_f32_e32 v24, v24, v171
	s_waitcnt lgkmcnt(3)
	v_add_f32_e32 v23, v23, v172
	s_waitcnt lgkmcnt(2)
	v_add_f32_e32 v3, v3, v173
	s_waitcnt lgkmcnt(1)
	v_add_f32_e32 v22, v22, v174
	s_waitcnt lgkmcnt(0)
	v_add_f32_e32 v1, v1, v175
	ds_bpermute_b32 v160, v82, v0
	ds_bpermute_b32 v161, v82, v34
	ds_bpermute_b32 v162, v82, v8
	ds_bpermute_b32 v163, v82, v9
	ds_bpermute_b32 v164, v82, v35
	ds_bpermute_b32 v165, v82, v65
	ds_bpermute_b32 v166, v82, v61
	ds_bpermute_b32 v167, v82, v63
	s_waitcnt lgkmcnt(7)
	v_add_f32_e32 v0, v0, v160
	s_waitcnt lgkmcnt(6)
	v_add_f32_e32 v34, v34, v161
	s_waitcnt lgkmcnt(5)
	v_add_f32_e32 v8, v8, v162
	s_waitcnt lgkmcnt(4)
	v_add_f32_e32 v9, v9, v163
	s_waitcnt lgkmcnt(3)
	v_add_f32_e32 v35, v35, v164
	s_waitcnt lgkmcnt(2)
	v_add_f32_e32 v65, v65, v165
	s_waitcnt lgkmcnt(1)
	v_add_f32_e32 v61, v61, v166
	s_waitcnt lgkmcnt(0)
	v_add_f32_e32 v63, v63, v167
	ds_bpermute_b32 v168, v82, v27
	ds_bpermute_b32 v169, v82, v26
	ds_bpermute_b32 v170, v82, v25
	ds_bpermute_b32 v171, v82, v24
	ds_bpermute_b32 v172, v82, v23
	ds_bpermute_b32 v173, v82, v3
	ds_bpermute_b32 v174, v82, v22
	ds_bpermute_b32 v175, v82, v1
	s_waitcnt lgkmcnt(7)
	v_add_f32_e32 v27, v27, v168
	s_waitcnt lgkmcnt(6)
	v_add_f32_e32 v26, v26, v169
	s_waitcnt lgkmcnt(5)
	v_add_f32_e32 v25, v25, v170
	s_waitcnt lgkmcnt(4)
	v_add_f32_e32 v24, v24, v171
	s_waitcnt lgkmcnt(3)
	v_add_f32_e32 v23, v23, v172
	s_waitcnt lgkmcnt(2)
	v_add_f32_e32 v3, v3, v173
	s_waitcnt lgkmcnt(1)
	v_add_f32_e32 v22, v22, v174
	s_waitcnt lgkmcnt(0)
	v_add_f32_e32 v1, v1, v175
	ds_bpermute_b32 v160, v83, v0
	ds_bpermute_b32 v161, v83, v34
	ds_bpermute_b32 v162, v83, v8
	ds_bpermute_b32 v163, v83, v9
	ds_bpermute_b32 v164, v83, v35
	ds_bpermute_b32 v165, v83, v65
	ds_bpermute_b32 v166, v83, v61
	ds_bpermute_b32 v167, v83, v63
	s_waitcnt lgkmcnt(7)
	v_add_f32_e32 v0, v0, v160
	s_waitcnt lgkmcnt(6)
	v_add_f32_e32 v34, v34, v161
	s_waitcnt lgkmcnt(5)
	v_add_f32_e32 v8, v8, v162
	s_waitcnt lgkmcnt(4)
	v_add_f32_e32 v9, v9, v163
	s_waitcnt lgkmcnt(3)
	v_add_f32_e32 v35, v35, v164
	s_waitcnt lgkmcnt(2)
	v_add_f32_e32 v65, v65, v165
	s_waitcnt lgkmcnt(1)
	v_add_f32_e32 v61, v61, v166
	s_waitcnt lgkmcnt(0)
	v_add_f32_e32 v63, v63, v167
	ds_bpermute_b32 v168, v83, v27
	ds_bpermute_b32 v169, v83, v26
	ds_bpermute_b32 v170, v83, v25
	ds_bpermute_b32 v171, v83, v24
	ds_bpermute_b32 v172, v83, v23
	ds_bpermute_b32 v173, v83, v3
	ds_bpermute_b32 v174, v83, v22
	ds_bpermute_b32 v175, v83, v1
	s_waitcnt lgkmcnt(7)
; template <bool COMBINE, bool ROUTE, bool FINAL, bool OUT8 = false, bool DUMMY = false> ...
;     ...
;                 for (int e = 0; e < 16; ++e) { lg[e] = wave_sum(lg[e]); sc_[e] = 1.f / (1.f + expf(-lg[e])); sel[e] = sc_[e] + rb[e]; }
	v_add_f32_e32 v27, v27, v168
	s_waitcnt lgkmcnt(6)
	v_add_f32_e32 v26, v26, v169
	s_waitcnt lgkmcnt(5)
	v_add_f32_e32 v25, v25, v170
	s_waitcnt lgkmcnt(4)
	v_add_f32_e32 v24, v24, v171
	s_waitcnt lgkmcnt(3)
	v_add_f32_e32 v23, v23, v172
	s_waitcnt lgkmcnt(2)
	v_add_f32_e32 v3, v3, v173
	s_waitcnt lgkmcnt(1)
	v_add_f32_e32 v22, v22, v174
	s_waitcnt lgkmcnt(0)
	v_add_f32_e32 v1, v1, v175
	ds_bpermute_b32 v176, v78, v0
	ds_bpermute_b32 v176, v78, v34
	global_load_dwordx4 v[16:19], v41, s[42:43]
	s_waitcnt lgkmcnt(12)
	s_nop 0
	s_waitcnt lgkmcnt(12)
	v_mov_b32_e32 v4, v34
	ds_bpermute_b32 v176, v79, v0
	ds_bpermute_b32 v176, v79, v4
	s_waitcnt lgkmcnt(12)
	s_nop 0
	s_waitcnt lgkmcnt(12)
	s_nop 0
	ds_bpermute_b32 v176, v80, v0
	ds_bpermute_b32 v176, v80, v4
	s_waitcnt lgkmcnt(12)
	s_nop 0
	s_waitcnt lgkmcnt(12)
	s_nop 0
	ds_bpermute_b32 v176, v81, v0
	ds_bpermute_b32 v176, v81, v4
	s_waitcnt lgkmcnt(12)
	s_nop 0
	s_waitcnt lgkmcnt(12)
	s_nop 0
	ds_bpermute_b32 v176, v82, v0
	ds_bpermute_b32 v176, v82, v4
	s_waitcnt lgkmcnt(12)
	s_nop 0
	s_waitcnt lgkmcnt(12)
	s_nop 0
	ds_bpermute_b32 v176, v83, v0
	ds_bpermute_b32 v176, v83, v4
	s_waitcnt lgkmcnt(12)
	s_nop 0
	s_waitcnt lgkmcnt(12)
	v_mov_b32_e32 v5, v4
	v_mul_f32_e32 v4, 0xbfb8aa3b, v0
	v_fma_f32 v7, v0, s58, -v4
	v_rndne_f32_e32 v10, v4
	v_mul_f32_e32 v6, 0xbfb8aa3b, v5
	v_fmac_f32_e32 v7, 0xb2a5705f, v0
	v_sub_f32_e32 v4, v4, v10
	v_fma_f32 v11, v5, s58, -v6
	v_rndne_f32_e32 v12, v6
	v_add_f32_e32 v4, v4, v7
	v_cvt_i32_f32_e32 v10, v10
	v_fmac_f32_e32 v11, 0xb2a5705f, v5
	v_sub_f32_e32 v6, v6, v12
	v_exp_f32_e32 v4, v4
	v_add_f32_e32 v6, v6, v11
	v_cvt_i32_f32_e32 v12, v12
	v_exp_f32_e32 v6, v6
	ds_bpermute_b32 v176, v78, v8
	v_ldexp_f32 v4, v4, v10
	v_cmp_nlt_f32_e32 vcc, s59, v0
	v_ldexp_f32 v6, v6, v12
	global_load_dwordx4 v[12:15], v41, s[42:43] offset:16
	v_cndmask_b32_e32 v4, 0, v4, vcc
	v_cmp_ngt_f32_e32 vcc, s61, v0
	s_waitcnt lgkmcnt(12)
	v_mov_b32_e32 v7, v8
	ds_bpermute_b32 v176, v79, v7
	v_cndmask_b32_e32 v4, v152, v4, vcc
	v_cmp_nlt_f32_e32 vcc, s59, v5
	s_waitcnt lgkmcnt(12)
	s_nop 0
	v_cndmask_b32_e32 v0, 0, v6, vcc
	v_cmp_ngt_f32_e32 vcc, s61, v5
	ds_bpermute_b32 v176, v80, v7
	s_waitcnt lgkmcnt(12)
	s_nop 0
	v_cndmask_b32_e32 v5, v152, v0, vcc
	v_pk_add_f32 v[4:5], v[4:5], 1.0 op_sel_hi:[1,0]
	ds_bpermute_b32 v176, v81, v7
	v_div_scale_f32 v0, s[6:7], v5, v5, 1.0
	v_rcp_f32_e32 v6, v0
	s_nop 0
	v_fma_f32 v10, -v0, v6, 1.0
	v_fmac_f32_e32 v6, v10, v6
	v_div_scale_f32 v10, vcc, 1.0, v5, 1.0
	v_mul_f32_e32 v11, v10, v6
	v_fma_f32 v20, -v0, v11, v10
	v_fmac_f32_e32 v11, v20, v6
	v_fma_f32 v0, -v0, v11, v10
	v_div_scale_f32 v10, s[6:7], v4, v4, 1.0
	v_rcp_f32_e32 v20, v10
	v_div_fmas_f32 v0, v0, v6, v11
	v_div_fixup_f32 v21, v0, v5, 1.0
	v_div_scale_f32 v6, vcc, 1.0, v4, 1.0
	v_fma_f32 v0, -v10, v20, 1.0
	v_fmac_f32_e32 v20, v0, v20
	s_waitcnt lgkmcnt(12)
	v_mov_b32_e32 v0, v7
	ds_bpermute_b32 v176, v82, v0
	v_mul_f32_e32 v7, v6, v20
	v_fma_f32 v8, -v10, v7, v6
	v_fmac_f32_e32 v7, v8, v20
	v_fma_f32 v6, -v10, v7, v6
	s_waitcnt lgkmcnt(12)
	s_nop 0
	ds_bpermute_b32 v176, v83, v0
	ds_bpermute_b32 v176, v78, v9
	v_div_fmas_f32 v6, v6, v20, v7
	v_div_fixup_f32 v20, v6, v4, 1.0
	s_waitcnt vmcnt(1)
	v_pk_add_f32 v[16:17], v[16:17], v[20:21]
	s_waitcnt lgkmcnt(12)
	s_nop 0
	v_mul_f32_e32 v5, 0xbfb8aa3b, v0
	v_fma_f32 v7, v0, s58, -v5
	v_rndne_f32_e32 v8, v5
	v_fmac_f32_e32 v7, 0xb2a5705f, v0
	v_sub_f32_e32 v5, v5, v8
	s_waitcnt lgkmcnt(12)
	v_mov_b32_e32 v30, v9
	v_add_f32_e32 v5, v5, v7
	ds_bpermute_b32 v176, v79, v30
	v_exp_f32_e32 v28, v5
	v_cvt_i32_f32_e32 v29, v8
	v_cmp_nlt_f32_e32 vcc, s59, v0
	global_load_dwordx4 v[4:7], v41, s[42:43] offset:48
	global_load_dwordx4 v[8:11], v41, s[42:43] offset:32
	v_ldexp_f32 v28, v28, v29
	s_waitcnt lgkmcnt(12)
	v_mov_b32_e32 v29, v30
	ds_bpermute_b32 v176, v80, v29
	v_cndmask_b32_e32 v28, 0, v28, vcc
	v_cmp_ngt_f32_e32 vcc, s61, v0
	s_nop 1
	v_cndmask_b32_e32 v0, v152, v28, vcc
	s_waitcnt lgkmcnt(12)
	v_mov_b32_e32 v28, v29
	ds_bpermute_b32 v176, v81, v28
	v_add_f32_e32 v0, 1.0, v0
	v_div_scale_f32 v30, s[6:7], v0, v0, 1.0
	v_rcp_f32_e32 v31, v30
	s_waitcnt lgkmcnt(12)
	s_nop 0
	ds_bpermute_b32 v176, v82, v28
	v_fma_f32 v32, -v30, v31, 1.0
	v_fmac_f32_e32 v31, v32, v31
	v_div_scale_f32 v32, vcc, 1.0, v0, 1.0
	s_waitcnt lgkmcnt(12)
	s_nop 0
	ds_bpermute_b32 v176, v83, v28
	v_mul_f32_e32 v33, v32, v31
	v_fma_f32 v34, -v30, v33, v32
	v_fmac_f32_e32 v33, v34, v31
	v_fma_f32 v30, -v30, v33, v32
	s_waitcnt lgkmcnt(12)
	s_nop 0
	v_mul_f32_e32 v29, 0xbfb8aa3b, v28
	v_fma_f32 v32, v28, s58, -v29
	v_rndne_f32_e32 v34, v29
	v_fmac_f32_e32 v32, 0xb2a5705f, v28
	v_sub_f32_e32 v29, v29, v34
	v_add_f32_e32 v29, v29, v32
	v_cvt_i32_f32_e32 v32, v34
	ds_bpermute_b32 v176, v78, v35
	v_div_fmas_f32 v30, v30, v31, v33
	v_exp_f32_e32 v29, v29
	v_div_fixup_f32 v0, v30, v0, 1.0
	v_cmp_nlt_f32_e32 vcc, s59, v28
	s_waitcnt lgkmcnt(12)
	v_mov_b32_e32 v30, v35
	ds_bpermute_b32 v176, v79, v30
	v_ldexp_f32 v29, v29, v32
	v_cndmask_b32_e32 v29, 0, v29, vcc
	v_cmp_ngt_f32_e32 vcc, s61, v28
	v_add_f32_e32 v67, v18, v0
	ds_bpermute_b32 v176, v78, v65
	v_cndmask_b32_e32 v28, v152, v29, vcc
	s_waitcnt lgkmcnt(12)
	v_mov_b32_e32 v29, v30
	ds_bpermute_b32 v176, v80, v29
	v_add_f32_e32 v31, 1.0, v28
	v_div_scale_f32 v28, s[6:7], v31, v31, 1.0
	v_rcp_f32_e32 v32, v28
	s_waitcnt lgkmcnt(12)
	s_nop 0
	ds_bpermute_b32 v176, v81, v29
	v_mov_b32_e32 v18, v65
	v_fma_f32 v33, -v28, v32, 1.0
	v_fmac_f32_e32 v32, v33, v32
	ds_bpermute_b32 v176, v79, v18
	s_waitcnt lgkmcnt(12)
	s_nop 0
	ds_bpermute_b32 v176, v82, v29
	v_div_scale_f32 v34, vcc, 1.0, v31, 1.0
	s_waitcnt lgkmcnt(12)
; template <bool COMBINE, bool ROUTE, bool FINAL, bool OUT8 = false, bool DUMMY = false> ...
;     ...
;                 for (int e = 0; e < 16; ++e) { lg[e] = wave_sum(lg[e]); sc_[e] = 1.f / (1.f + expf(-lg[e])); sel[e] = sc_[e] + rb[e]; }
	s_nop 0
	ds_bpermute_b32 v176, v80, v18
	s_waitcnt lgkmcnt(12)
	s_nop 0
	ds_bpermute_b32 v176, v83, v29
	v_mul_f32_e32 v35, v34, v32
	v_fma_f32 v40, -v28, v35, v34
	s_waitcnt lgkmcnt(12)
	s_nop 0
	v_fmac_f32_e32 v35, v40, v32
	s_waitcnt lgkmcnt(12)
	s_nop 0
	ds_bpermute_b32 v176, v81, v18
	v_mul_f32_e32 v33, 0xbfb8aa3b, v29
	v_fma_f32 v40, v29, s58, -v33
	v_rndne_f32_e32 v59, v33
	v_fmac_f32_e32 v40, 0xb2a5705f, v29
	s_waitcnt lgkmcnt(12)
	s_nop 0
	ds_bpermute_b32 v176, v82, v18
	v_sub_f32_e32 v33, v33, v59
	v_add_f32_e32 v33, v33, v40
	v_exp_f32_e32 v33, v33
	v_cvt_i32_f32_e32 v40, v59
	s_waitcnt lgkmcnt(12)
	s_nop 0
	ds_bpermute_b32 v176, v83, v18
	v_fma_f32 v28, -v28, v35, v34
	v_div_fmas_f32 v32, v28, v32, v35
	v_ldexp_f32 v28, v33, v40
	v_cmp_nlt_f32_e32 vcc, s59, v29
	s_waitcnt lgkmcnt(12)
	s_nop 0
	v_mul_f32_e32 v30, 0xbfb8aa3b, v18
	v_fma_f32 v33, v18, s58, -v30
	v_rndne_f32_e32 v34, v30
	v_fmac_f32_e32 v33, 0xb2a5705f, v18
	v_sub_f32_e32 v30, v30, v34
	v_add_f32_e32 v30, v30, v33
	v_exp_f32_e32 v30, v30
	v_cvt_i32_f32_e32 v33, v34
	v_cndmask_b32_e32 v28, 0, v28, vcc
	v_cmp_ngt_f32_e32 vcc, s61, v29
	ds_bpermute_b32 v176, v78, v61
	v_ldexp_f32 v29, v30, v33
	v_cndmask_b32_e32 v28, v152, v28, vcc
	v_cmp_nlt_f32_e32 vcc, s59, v18
	s_nop 1
	v_cndmask_b32_e32 v29, 0, v29, vcc
	v_cmp_ngt_f32_e32 vcc, s61, v18
	ds_bpermute_b32 v176, v78, v63
	s_waitcnt lgkmcnt(12)
	v_mov_b32_e32 v18, v63
	v_cndmask_b32_e32 v29, v152, v29, vcc
	v_pk_add_f32 v[28:29], v[28:29], 1.0 op_sel_hi:[1,0]
	ds_bpermute_b32 v176, v79, v18
	v_div_scale_f32 v30, s[6:7], v29, v29, 1.0
	v_rcp_f32_e32 v33, v30
	v_div_fixup_f32 v63, v32, v31, 1.0
	v_add_f32_e32 v65, v19, v63
	s_waitcnt lgkmcnt(12)
	s_nop 0
	v_fma_f32 v19, -v30, v33, 1.0
	v_fmac_f32_e32 v33, v19, v33
	ds_bpermute_b32 v176, v80, v18
	v_div_scale_f32 v31, vcc, 1.0, v29, 1.0
	v_mul_f32_e32 v32, v31, v33
	v_fma_f32 v34, -v30, v32, v31
	s_waitcnt lgkmcnt(12)
	s_nop 0
	ds_bpermute_b32 v176, v81, v18
	v_fmac_f32_e32 v32, v34, v33
	v_fma_f32 v30, -v30, v32, v31
	v_div_scale_f32 v31, s[6:7], v28, v28, 1.0
	s_waitcnt lgkmcnt(12)
	s_nop 0
	ds_bpermute_b32 v176, v82, v18
	v_div_fmas_f32 v19, v30, v33, v32
	v_rcp_f32_e32 v34, v31
	v_div_fixup_f32 v19, v19, v29, 1.0
	s_waitcnt lgkmcnt(12)
	s_nop 0
	ds_bpermute_b32 v176, v83, v18
	v_fma_f32 v29, -v31, v34, 1.0
	v_fmac_f32_e32 v34, v29, v34
	v_div_scale_f32 v29, vcc, 1.0, v28, 1.0
	s_waitcnt lgkmcnt(12)
	s_nop 0
	v_mul_f32_e32 v30, 0xbfb8aa3b, v18
	v_fma_f32 v33, v18, s58, -v30
	v_rndne_f32_e32 v35, v30
	v_fmac_f32_e32 v33, 0xb2a5705f, v18
	v_sub_f32_e32 v30, v30, v35
	v_add_f32_e32 v30, v30, v33
	v_cvt_i32_f32_e32 v33, v35
	v_mov_b32_e32 v35, v61
	ds_bpermute_b32 v176, v79, v35
	v_mul_f32_e32 v32, v29, v34
	v_exp_f32_e32 v30, v30
	v_fma_f32 v59, -v31, v32, v29
	v_fmac_f32_e32 v32, v59, v34
	v_fma_f32 v29, -v31, v32, v29
	s_waitcnt lgkmcnt(12)
	v_mov_b32_e32 v31, v35
	v_ldexp_f32 v30, v30, v33
	ds_bpermute_b32 v176, v80, v31
	v_cmp_nlt_f32_e64 s[6:7], s59, v18
	s_nop 1
	v_cndmask_b32_e64 v30, 0, v30, s[6:7]
	v_cmp_ngt_f32_e64 s[6:7], s61, v18
	s_nop 1
	v_cndmask_b32_e64 v18, v152, v30, s[6:7]
	s_waitcnt lgkmcnt(12)
	v_mov_b32_e32 v30, v31
	ds_bpermute_b32 v176, v81, v30
	v_add_f32_e32 v33, 1.0, v18
	v_div_fmas_f32 v18, v29, v34, v32
	v_div_fixup_f32 v18, v18, v28, 1.0
	s_waitcnt vmcnt(2)
	v_pk_add_f32 v[72:73], v[12:13], v[18:19]
	s_waitcnt lgkmcnt(12)
	s_nop 0
	ds_bpermute_b32 v176, v82, v30
	v_div_scale_f32 v35, s[6:7], v33, v33, 1.0
	v_rcp_f32_e32 v40, v35
	v_cmp_nlg_f32_e64 s[12:13], s62, v72
	s_waitcnt lgkmcnt(12)
	v_mov_b32_e32 v13, v30
	ds_bpermute_b32 v176, v83, v13
	v_fma_f32 v12, -v35, v40, 1.0
	v_fmac_f32_e32 v40, v12, v40
	v_div_scale_f32 v12, vcc, 1.0, v33, 1.0
	s_waitcnt lgkmcnt(12)
	s_nop 0
	v_mul_f32_e32 v28, 0xbfb8aa3b, v13
	v_fma_f32 v30, v13, s58, -v28
	v_rndne_f32_e32 v31, v28
	v_fmac_f32_e32 v30, 0xb2a5705f, v13
	v_sub_f32_e32 v28, v28, v31
	v_add_f32_e32 v28, v28, v30
	v_mul_f32_e32 v29, v12, v40
	v_exp_f32_e32 v28, v28
	v_cvt_i32_f32_e32 v30, v31
	v_fma_f32 v31, -v35, v29, v12
	v_fmac_f32_e32 v29, v31, v40
	v_fma_f32 v12, -v35, v29, v12
	v_ldexp_f32 v28, v28, v30
	v_cmp_nlt_f32_e64 s[6:7], s59, v13
	v_div_fmas_f32 v12, v12, v40, v29
	v_div_fixup_f32 v32, v12, v33, 1.0
	v_cndmask_b32_e64 v28, 0, v28, s[6:7]
	v_cmp_ngt_f32_e64 s[6:7], s61, v13
	v_add_f32_e32 v61, v14, v32
	ds_bpermute_b32 v176, v78, v27
	v_cndmask_b32_e64 v13, v152, v28, s[6:7]
	v_add_f32_e32 v13, 1.0, v13
	v_div_scale_f32 v28, s[6:7], v13, v13, 1.0
	v_rcp_f32_e32 v30, v28
	s_waitcnt lgkmcnt(12)
	v_mov_b32_e32 v14, v27
	ds_bpermute_b32 v176, v79, v14
	ds_bpermute_b32 v176, v78, v26
	v_fma_f32 v12, -v28, v30, 1.0
	v_fmac_f32_e32 v30, v12, v30
	v_div_scale_f32 v12, vcc, 1.0, v13, 1.0
	v_mul_f32_e32 v29, v12, v30
	v_fma_f32 v31, -v28, v29, v12
	v_fmac_f32_e32 v29, v31, v30
	s_waitcnt lgkmcnt(12)
	s_nop 0
	s_waitcnt lgkmcnt(12)
	s_nop 0
	v_fma_f32 v12, -v28, v29, v12
	ds_bpermute_b32 v176, v80, v14
	ds_bpermute_b32 v176, v79, v26
	v_div_fmas_f32 v12, v12, v30, v29
	v_div_fixup_f32 v34, v12, v13, 1.0
	v_add_f32_e32 v69, v15, v34
	s_waitcnt lgkmcnt(12)
	v_mov_b32_e32 v12, v14
	s_waitcnt lgkmcnt(12)
	v_mov_b32_e32 v14, v26
	ds_bpermute_b32 v176, v81, v12
	ds_bpermute_b32 v176, v80, v14
	ds_bpermute_b32 v176, v78, v25
	v_cmp_gt_f32_e32 vcc, v17, v16
	v_cmp_nlg_f32_e64 s[6:7], s62, v16
	s_waitcnt lgkmcnt(12)
	s_nop 0
	s_waitcnt lgkmcnt(12)
	s_nop 0
	s_waitcnt lgkmcnt(12)
	s_nop 0
	ds_bpermute_b32 v176, v82, v12
	ds_bpermute_b32 v176, v81, v14
	ds_bpermute_b32 v176, v79, v25
	s_waitcnt lgkmcnt(12)
	v_mov_b32_e32 v15, v12
	s_waitcnt lgkmcnt(12)
	v_mov_b32_e32 v12, v14
	s_waitcnt lgkmcnt(12)
; template <bool COMBINE, bool ROUTE, bool FINAL, bool OUT8 = false, bool DUMMY = false> ...
;     ...
;                 for (int e = 0; e < 16; ++e) { lg[e] = wave_sum(lg[e]); sc_[e] = 1.f / (1.f + expf(-lg[e])); sel[e] = sc_[e] + rb[e]; }
;                 float gsv[4], gw1[4], gw2[4]; int gi1[4], gi2[4];
; #pragma unroll
;                 for (int gq = 0; gq < 4; ++gq) {
;                     float m1 = sel[4 * gq]; int i1 = 0; float s1 = sc_[4 * gq];
; #pragma unroll
;                     for (int i = 1; i < 4; ++i) if (sel[4 * gq + i] > m1) { m1 = sel[4 * gq + i]; i1 = i; s1 = sc_[4 * gq + i]; }
;                     float m2 = -INFINITY; int i2 = 0; float s2 = 0.f;
; #pragma unroll
;                     for (int i = 0; i < 4; ++i) if (i != i1 && sel[4 * gq + i] > m2) { m2 = sel[4 * gq + i]; i2 = i; s2 = sc_[4 * gq + i]; }
;                     gsv[gq] = m1 + m2; gi1[gq] = 4 * gq + i1; gi2[gq] = 4 * gq + i2; gw1[gq] = s1; gw2[gq] = s2;
;                 }
;                 float bv = gsv[0]; int e0 = gi1[0], e1 = gi2[0]; float w0 = gw1[0], w1 = gw2[0];
; #pragma unroll
;                 for (int gq = 1; gq < 4; ++gq) if (gsv[gq] > bv) { bv = gsv[gq]; e0 = gi1[gq]; e1 = gi2[gq]; w0 = gw1[gq]; w1 = gw2[gq]; }
	v_mov_b32_e32 v14, v25
	ds_bpermute_b32 v176, v78, v24
	ds_bpermute_b32 v176, v78, v23
	ds_bpermute_b32 v176, v80, v14
	ds_bpermute_b32 v176, v82, v12
	ds_bpermute_b32 v176, v83, v15
	s_waitcnt lgkmcnt(12)
	s_nop 0
	s_waitcnt lgkmcnt(12)
	v_mov_b32_e32 v13, v23
	s_waitcnt lgkmcnt(12)
	s_nop 0
	ds_bpermute_b32 v176, v79, v24
	ds_bpermute_b32 v176, v79, v13
	s_waitcnt lgkmcnt(12)
	v_mov_b32_e32 v40, v12
	ds_bpermute_b32 v176, v81, v14
	ds_bpermute_b32 v176, v83, v40
	s_waitcnt lgkmcnt(12)
	v_mov_b32_e32 v12, v24
	s_waitcnt lgkmcnt(12)
	s_nop 0
	ds_bpermute_b32 v176, v80, v12
	ds_bpermute_b32 v176, v80, v13
	s_waitcnt lgkmcnt(12)
	s_nop 0
	ds_bpermute_b32 v176, v82, v14
	s_waitcnt lgkmcnt(12)
	s_nop 0
	s_waitcnt lgkmcnt(12)
	s_nop 0
	ds_bpermute_b32 v176, v81, v12
	ds_bpermute_b32 v176, v81, v13
	s_waitcnt lgkmcnt(12)
	s_nop 0
	ds_bpermute_b32 v176, v83, v14
	s_waitcnt lgkmcnt(12)
	s_nop 0
	s_waitcnt lgkmcnt(12)
	s_nop 0
	ds_bpermute_b32 v176, v82, v12
	ds_bpermute_b32 v176, v82, v13
	s_waitcnt lgkmcnt(12)
	v_mov_b32_e32 v26, v12
	ds_bpermute_b32 v176, v78, v3
	s_waitcnt lgkmcnt(12)
	v_mov_b32_e32 v30, v13
	ds_bpermute_b32 v176, v78, v22
	ds_bpermute_b32 v176, v78, v1
	ds_bpermute_b32 v176, v83, v30
	s_waitcnt lgkmcnt(12)
	s_nop 0
	ds_bpermute_b32 v176, v79, v3
	s_waitcnt lgkmcnt(12)
	v_mov_b32_e32 v13, v22
	s_waitcnt lgkmcnt(12)
	s_nop 0
	ds_bpermute_b32 v176, v79, v13
	ds_bpermute_b32 v176, v79, v1
	s_waitcnt lgkmcnt(12)
	s_nop 0
	ds_bpermute_b32 v176, v80, v3
	ds_bpermute_b32 v176, v83, v26
	s_waitcnt lgkmcnt(12)
	s_nop 0
	s_waitcnt lgkmcnt(12)
	s_nop 0
	ds_bpermute_b32 v176, v80, v13
	ds_bpermute_b32 v176, v80, v1
	s_waitcnt lgkmcnt(12)
	s_nop 0
	ds_bpermute_b32 v176, v81, v3
	s_waitcnt lgkmcnt(12)
	s_nop 0
	s_waitcnt lgkmcnt(12)
	s_nop 0
	ds_bpermute_b32 v176, v81, v13
	ds_bpermute_b32 v176, v81, v1
	s_waitcnt lgkmcnt(12)
	s_nop 0
	ds_bpermute_b32 v176, v82, v3
	s_waitcnt lgkmcnt(12)
	s_nop 0
	s_waitcnt lgkmcnt(12)
	s_nop 0
	ds_bpermute_b32 v176, v82, v13
	ds_bpermute_b32 v176, v82, v1
	s_waitcnt lgkmcnt(12)
	v_mov_b32_e32 v24, v3
	v_cndmask_b32_e32 v12, v16, v17, vcc
	v_cndmask_b32_e64 v3, 0, 1, vcc
	s_waitcnt lgkmcnt(12)
	v_mov_b32_e32 v28, v13
	s_waitcnt lgkmcnt(12)
	v_mov_b32_e32 v22, v1
	v_cndmask_b32_e32 v1, v20, v21, vcc
	v_cmp_gt_f32_e32 vcc, v67, v12
	ds_bpermute_b32 v176, v83, v28
	ds_bpermute_b32 v176, v83, v24
	v_cndmask_b32_e32 v12, v12, v67, vcc
	v_cndmask_b32_e32 v1, v1, v0, vcc
	v_cndmask_b32_e64 v13, v3, 2, vcc
	v_cmp_ngt_f32_e32 vcc, v65, v12
	ds_bpermute_b32 v176, v83, v22
	s_nop 0
	v_cndmask_b32_e32 v71, v65, v12, vcc
	v_cndmask_b32_e32 v12, 3, v13, vcc
	v_cmp_eq_u32_e64 s[8:9], 0, v12
	s_or_b64 s[6:7], s[8:9], s[6:7]
	v_cndmask_b32_e32 v3, v63, v1, vcc
	v_cndmask_b32_e64 v1, v16, v153, s[6:7]
	v_cndmask_b32_e64 v13, v20, 0, s[6:7]
	v_cmp_ne_u32_e64 s[6:7], 1, v12
	v_cmp_gt_f32_e64 s[8:9], v17, v1
	s_and_b64 s[6:7], s[6:7], s[8:9]
	v_cndmask_b32_e64 v1, v1, v17, s[6:7]
	v_cndmask_b32_e64 v16, 0, 1, s[6:7]
	v_cndmask_b32_e64 v13, v13, v21, s[6:7]
	v_cmp_ne_u32_e64 s[6:7], 2, v12
	v_cmp_gt_f32_e64 s[8:9], v67, v1
	s_and_b64 s[6:7], s[6:7], s[8:9]
	v_cndmask_b32_e64 v1, v1, v67, s[6:7]
	v_cndmask_b32_e64 v16, v16, 2, s[6:7]
	v_cndmask_b32_e64 v0, v13, v0, s[6:7]
	v_cmp_gt_f32_e64 s[6:7], v65, v1
	s_and_b64 vcc, vcc, s[6:7]
	v_cndmask_b32_e32 v17, v1, v65, vcc
	v_cndmask_b32_e64 v1, v16, 3, vcc
	v_cndmask_b32_e32 v13, v0, v63, vcc
	v_cmp_gt_f32_e32 vcc, v73, v72
	v_add_f32_e32 v16, v71, v17
	s_nop 0
	v_cndmask_b32_e32 v17, v72, v73, vcc
	v_cmp_gt_f32_e64 s[6:7], v61, v17
	v_cndmask_b32_e64 v0, 0, 1, vcc
	s_nop 0
	v_cndmask_b32_e64 v20, v17, v61, s[6:7]
	v_cndmask_b32_e64 v0, v0, 2, s[6:7]
	v_cmp_ngt_f32_e64 s[8:9], v69, v20
	s_nop 1
	v_cndmask_b32_e64 v17, 3, v0, s[8:9]
	v_cmp_eq_u32_e64 s[10:11], 0, v17
	s_or_b64 s[10:11], s[10:11], s[12:13]
	v_cndmask_b32_e64 v0, v69, v20, s[8:9]
	v_cndmask_b32_e64 v20, v72, v153, s[10:11]
	v_cmp_ne_u32_e64 s[12:13], 1, v17
	v_cmp_gt_f32_e64 s[14:15], v73, v20
	s_and_b64 s[12:13], s[12:13], s[14:15]
	v_cndmask_b32_e64 v20, v20, v73, s[12:13]
	v_cmp_ne_u32_e64 s[14:15], 2, v17
	v_cmp_gt_f32_e64 s[16:17], v61, v20
	s_and_b64 s[14:15], s[14:15], s[16:17]
	v_cndmask_b32_e64 v20, v20, v61, s[14:15]
	v_cmp_gt_f32_e64 s[16:17], v69, v20
	s_and_b64 s[16:17], s[8:9], s[16:17]
	s_nop 0
	v_cndmask_b32_e64 v20, v20, v69, s[16:17]
	v_add_f32_e32 v20, v0, v20
	v_cmp_gt_f32_e64 s[18:19], v20, v16
	s_and_saveexec_b64 s[56:57], s[18:19]
	s_cbranch_execz .LBB0_525
	v_cndmask_b32_e64 v0, 4, 5, s[12:13]
	v_cndmask_b32_e64 v0, v0, 6, s[14:15]
	v_cndmask_b32_e64 v1, v0, 7, s[16:17]
	v_cndmask_b32_e64 v0, v18, 0, s[10:11]
	v_cndmask_b32_e64 v0, v0, v19, s[12:13]
	v_cndmask_b32_e64 v0, v0, v32, s[14:15]
	v_cndmask_b32_e64 v13, v0, v34, s[16:17]
	v_cndmask_b32_e32 v0, v18, v19, vcc
	v_cndmask_b32_e64 v0, v0, v32, s[6:7]
	v_or_b32_e32 v12, 4, v17
	v_cndmask_b32_e64 v3, v34, v0, s[8:9]
	v_mov_b32_e32 v16, v20
; template <bool COMBINE, bool ROUTE, bool FINAL, bool OUT8 = false, bool DUMMY = false> ...
;     ...
;                 for (int e = 0; e < 16; ++e) { lg[e] = wave_sum(lg[e]); sc_[e] = 1.f / (1.f + expf(-lg[e])); sel[e] = sc_[e] + rb[e]; }
;                 float gsv[4], gw1[4], gw2[4]; int gi1[4], gi2[4];
; #pragma unroll
;                 for (int gq = 0; gq < 4; ++gq) {
;                     float m1 = sel[4 * gq]; int i1 = 0; float s1 = sc_[4 * gq];
; #pragma unroll
;                     for (int i = 1; i < 4; ++i) if (sel[4 * gq + i] > m1) { m1 = sel[4 * gq + i]; i1 = i; s1 = sc_[4 * gq + i]; }
;                     float m2 = -INFINITY; int i2 = 0; float s2 = 0.f;
; #pragma unroll
;                     for (int i = 0; i < 4; ++i) if (i != i1 && sel[4 * gq + i] > m2) { m2 = sel[4 * gq + i]; i2 = i; s2 = sc_[4 * gq + i]; }
;                     gsv[gq] = m1 + m2; gi1[gq] = 4 * gq + i1; gi2[gq] = 4 * gq + i2; gw1[gq] = s1; gw2[gq] = s2;
;                 }
;                 float bv = gsv[0]; int e0 = gi1[0], e1 = gi2[0]; float w0 = gw1[0], w1 = gw2[0];
; #pragma unroll
;                 for (int gq = 1; gq < 4; ++gq) if (gsv[gq] > bv) { bv = gsv[gq]; e0 = gi1[gq]; e1 = gi2[gq]; w0 = gw1[gq]; w1 = gw2[gq]; }
.LBB0_525:
	s_or_b64 exec, exec, s[56:57]
	v_mov_b32_e32 v0, v15
	v_mul_f32_e32 v15, 0xbfb8aa3b, v0
	v_fma_f32 v17, v0, s58, -v15
	v_rndne_f32_e32 v18, v15
	v_fmac_f32_e32 v17, 0xb2a5705f, v0
	v_sub_f32_e32 v15, v15, v18
	v_add_f32_e32 v15, v15, v17
	v_cvt_i32_f32_e32 v17, v18
	v_exp_f32_e32 v15, v15
	v_cmp_nlt_f32_e32 vcc, s59, v0
	s_nop 0
	v_ldexp_f32 v15, v15, v17
	v_mov_b32_e32 v17, v40
	v_mul_f32_e32 v18, 0xbfb8aa3b, v17
	v_fma_f32 v19, v17, s58, -v18
	v_rndne_f32_e32 v20, v18
	v_fmac_f32_e32 v19, 0xb2a5705f, v17
	v_sub_f32_e32 v18, v18, v20
	v_add_f32_e32 v18, v18, v19
	v_exp_f32_e32 v19, v18
	v_cvt_i32_f32_e32 v20, v20
	v_cndmask_b32_e32 v15, 0, v15, vcc
	v_cmp_ngt_f32_e32 vcc, s61, v0
	v_ldexp_f32 v0, v19, v20
	s_nop 0
	v_cndmask_b32_e32 v18, v152, v15, vcc
	v_cmp_nlt_f32_e32 vcc, s59, v17
	s_nop 1
	v_cndmask_b32_e32 v0, 0, v0, vcc
	v_cmp_ngt_f32_e32 vcc, s61, v17
	s_nop 1
	v_cndmask_b32_e32 v19, v152, v0, vcc
	v_pk_add_f32 v[18:19], v[18:19], 1.0 op_sel_hi:[1,0]
	s_nop 0
	v_div_scale_f32 v0, s[6:7], v19, v19, 1.0
	v_rcp_f32_e32 v15, v0
	s_nop 0
	v_fma_f32 v17, -v0, v15, 1.0
	v_fmac_f32_e32 v15, v17, v15
	v_div_scale_f32 v17, vcc, 1.0, v19, 1.0
	v_mul_f32_e32 v20, v17, v15
	v_fma_f32 v21, -v0, v20, v17
	v_fmac_f32_e32 v20, v21, v15
	v_fma_f32 v0, -v0, v20, v17
	v_div_scale_f32 v17, s[6:7], v18, v18, 1.0
	v_rcp_f32_e32 v21, v17
	v_div_fmas_f32 v0, v0, v15, v20
	v_mul_f32_e32 v20, 0xbfb8aa3b, v14
	v_fma_f32 v32, v14, s58, -v20
	v_rndne_f32_e32 v33, v20
	v_fmac_f32_e32 v32, 0xb2a5705f, v14
	v_sub_f32_e32 v20, v20, v33
	v_div_fixup_f32 v15, v0, v19, 1.0
	v_fma_f32 v0, -v17, v21, 1.0
	v_add_f32_e32 v20, v20, v32
	v_fmac_f32_e32 v21, v0, v21
	v_div_scale_f32 v0, vcc, 1.0, v18, 1.0
	v_exp_f32_e32 v20, v20
	v_cvt_i32_f32_e32 v32, v33
	v_mul_f32_e32 v19, v0, v21
	v_fma_f32 v33, -v17, v19, v0
	v_fmac_f32_e32 v19, v33, v21
	v_fma_f32 v0, -v17, v19, v0
	v_ldexp_f32 v17, v20, v32
	v_cmp_nlt_f32_e64 s[6:7], s59, v14
	v_div_fmas_f32 v0, v0, v21, v19
	s_nop 0
	v_cndmask_b32_e64 v17, 0, v17, s[6:7]
	v_cmp_ngt_f32_e64 s[6:7], s61, v14
	s_nop 1
	v_cndmask_b32_e64 v14, v152, v17, s[6:7]
	v_add_f32_e32 v17, 1.0, v14
	v_div_scale_f32 v20, s[6:7], v17, v17, 1.0
	v_div_fixup_f32 v14, v0, v18, 1.0
	v_rcp_f32_e32 v32, v20
	s_waitcnt vmcnt(0)
	v_pk_add_f32 v[18:19], v[8:9], v[14:15]
	v_mov_b32_e32 v9, v30
	v_mul_f32_e32 v21, 0xbfb8aa3b, v9
	v_fma_f32 v30, v9, s58, -v21
	v_rndne_f32_e32 v31, v21
	v_fmac_f32_e32 v30, 0xb2a5705f, v9
	v_sub_f32_e32 v21, v21, v31
	v_fma_f32 v0, -v20, v32, 1.0
	v_add_f32_e32 v21, v21, v30
	v_fmac_f32_e32 v32, v0, v32
	v_div_scale_f32 v0, vcc, 1.0, v17, 1.0
	v_exp_f32_e32 v21, v21
	v_cvt_i32_f32_e32 v30, v31
	v_mul_f32_e32 v8, v0, v32
	v_fma_f32 v31, -v20, v8, v0
	v_fmac_f32_e32 v8, v31, v32
	v_fma_f32 v0, -v20, v8, v0
	v_ldexp_f32 v20, v21, v30
	v_cmp_nlt_f32_e64 s[6:7], s59, v9
	v_div_fmas_f32 v0, v0, v32, v8
	v_div_fixup_f32 v8, v0, v17, 1.0
	v_cndmask_b32_e64 v20, 0, v20, s[6:7]
	v_cmp_ngt_f32_e64 s[6:7], s61, v9
	v_add_f32_e32 v0, v10, v8
	v_cmp_nlg_f32_e64 s[12:13], s62, v18
	v_cndmask_b32_e64 v9, v152, v20, s[6:7]
	v_add_f32_e32 v9, 1.0, v9
	v_div_scale_f32 v20, s[6:7], v9, v9, 1.0
	v_rcp_f32_e32 v21, v20
	s_nop 0
	v_fma_f32 v10, -v20, v21, 1.0
	v_fmac_f32_e32 v21, v10, v21
	v_div_scale_f32 v10, vcc, 1.0, v9, 1.0
	v_mul_f32_e32 v17, v10, v21
	v_fma_f32 v30, -v20, v17, v10
	v_fmac_f32_e32 v17, v30, v21
	v_fma_f32 v10, -v20, v17, v10
	v_div_fmas_f32 v10, v10, v21, v17
	v_cmp_gt_f32_e32 vcc, v19, v18
	v_div_fixup_f32 v9, v10, v9, 1.0
	v_add_f32_e32 v11, v11, v9
	v_cndmask_b32_e32 v17, v18, v19, vcc
	v_cmp_gt_f32_e64 s[6:7], v0, v17
	v_cndmask_b32_e64 v10, 0, 1, vcc
	s_nop 0
	v_cndmask_b32_e64 v17, v17, v0, s[6:7]
	v_cndmask_b32_e64 v10, v10, 2, s[6:7]
	v_cmp_ngt_f32_e64 s[8:9], v11, v17
	s_nop 1
	v_cndmask_b32_e64 v10, 3, v10, s[8:9]
	v_cmp_eq_u32_e64 s[10:11], 0, v10
	s_or_b64 s[12:13], s[10:11], s[12:13]
	v_cndmask_b32_e64 v18, v18, v153, s[12:13]
	v_cmp_ne_u32_e64 s[10:11], 1, v10
	v_cmp_gt_f32_e64 s[14:15], v19, v18
	s_and_b64 s[10:11], s[10:11], s[14:15]
	v_cndmask_b32_e64 v18, v18, v19, s[10:11]
	v_cmp_ne_u32_e64 s[14:15], 2, v10
	v_cmp_gt_f32_e64 s[16:17], v0, v18
	s_and_b64 s[14:15], s[14:15], s[16:17]
	v_cndmask_b32_e64 v0, v18, v0, s[14:15]
	v_cmp_gt_f32_e64 s[16:17], v11, v0
	s_and_b64 s[16:17], s[8:9], s[16:17]
	v_cndmask_b32_e64 v17, v11, v17, s[8:9]
	v_cndmask_b32_e64 v0, v0, v11, s[16:17]
	v_add_f32_e32 v11, v17, v0
	v_cmp_gt_f32_e64 s[18:19], v11, v16
	s_and_saveexec_b64 s[56:57], s[18:19]
	s_cbranch_execz .LBB0_527
	v_cndmask_b32_e32 v0, v14, v15, vcc
	v_cndmask_b32_e64 v0, v0, v8, s[6:7]
	v_cndmask_b32_e64 v3, v9, v0, s[8:9]
	v_cndmask_b32_e64 v0, v14, 0, s[12:13]
	v_cndmask_b32_e64 v0, v0, v15, s[10:11]
	v_cndmask_b32_e64 v0, v0, v8, s[14:15]
	v_cndmask_b32_e64 v13, v0, v9, s[16:17]
	v_cndmask_b32_e64 v0, 8, 9, s[10:11]
	v_cndmask_b32_e64 v0, v0, 10, s[14:15]
	v_or_b32_e32 v12, 8, v10
	v_cndmask_b32_e64 v1, v0, 11, s[16:17]
	v_mov_b32_e32 v16, v11
; #define LAS __attribute__((address_space(3)))
; template <bool COMBINE, bool ROUTE, bool FINAL, bool OUT8 = false, bool DUMMY = false> ...
;     ...
;                 for (int e = 0; e < 16; ++e) { lg[e] = wave_sum(lg[e]); sc_[e] = 1.f / (1.f + expf(-lg[e])); sel[e] = sc_[e] + rb[e]; }
;                 float gsv[4], gw1[4], gw2[4]; int gi1[4], gi2[4];
; #pragma unroll
;                 for (int gq = 0; gq < 4; ++gq) {
;                     float m1 = sel[4 * gq]; int i1 = 0; float s1 = sc_[4 * gq];
; #pragma unroll
;                     for (int i = 1; i < 4; ++i) if (sel[4 * gq + i] > m1) { m1 = sel[4 * gq + i]; i1 = i; s1 = sc_[4 * gq + i]; }
;                     float m2 = -INFINITY; int i2 = 0; float s2 = 0.f;
; #pragma unroll
;                     for (int i = 0; i < 4; ++i) if (i != i1 && sel[4 * gq + i] > m2) { m2 = sel[4 * gq + i]; i2 = i; s2 = sc_[4 * gq + i]; }
;                     gsv[gq] = m1 + m2; gi1[gq] = 4 * gq + i1; gi2[gq] = 4 * gq + i2; gw1[gq] = s1; gw2[gq] = s2;
;                 }
;                 float bv = gsv[0]; int e0 = gi1[0], e1 = gi2[0]; float w0 = gw1[0], w1 = gw2[0];
; #pragma unroll
;                 for (int gq = 1; gq < 4; ++gq) if (gsv[gq] > bv) { bv = gsv[gq]; e0 = gi1[gq]; e1 = gi2[gq]; w0 = gw1[gq]; w1 = gw2[gq]; }
;                 const float wsum = w0 + w1; w0 /= wsum; w1 /= wsum;
;                 if (lane == 0) {
;                     const int k = rslot++;
;                     const int l0 = (int)__hip_atomic_fetch_add(rt_cnt + e0, 1u, __ATOMIC_RELAXED, __HIP_MEMORY_SCOPE_WORKGROUP), l1 = (int)__hip_atomic_fetch_add(rt_cnt + e1, 1u, __ATOMIC_RELAXED, __HIP_MEMORY_SCOPE_WORKGROUP);
;                     LAS int* rr = rt_sel + (k * 8 + wave) * 8;
;                     rr[0] = m; rr[1] = e0; rr[2] = e1; rr[3] = l0; rr[4] = l1; ((LAS float*)rr)[5] = w0; ((LAS float*)rr)[6] = w1;
;                 }
.LBB0_527:
	s_or_b64 exec, exec, s[56:57]
	s_and_saveexec_b64 s[12:13], s[4:5]
	s_cbranch_execz .LBB0_520
	v_mov_b32_e32 v0, v26
	v_mul_f32_e32 v8, 0xbfb8aa3b, v0
	v_fma_f32 v9, v0, s58, -v8
	v_rndne_f32_e32 v10, v8
	v_fmac_f32_e32 v9, 0xb2a5705f, v0
	v_sub_f32_e32 v8, v8, v10
	v_add_f32_e32 v8, v8, v9
	v_cvt_i32_f32_e32 v9, v10
	v_exp_f32_e32 v8, v8
	v_cmp_nlt_f32_e32 vcc, s59, v0
	v_ldexp_f32 v8, v8, v9
	s_waitcnt lgkmcnt(12)
	v_mov_b32_e32 v9, v28
	v_mul_f32_e32 v10, 0xbfb8aa3b, v9
	v_fma_f32 v11, v9, s58, -v10
	v_rndne_f32_e32 v14, v10
	v_fmac_f32_e32 v11, 0xb2a5705f, v9
	v_sub_f32_e32 v10, v10, v14
	v_add_f32_e32 v10, v10, v11
	v_exp_f32_e32 v10, v10
	v_cvt_i32_f32_e32 v11, v14
	v_cndmask_b32_e32 v8, 0, v8, vcc
	v_cmp_ngt_f32_e32 vcc, s61, v0
	v_ldexp_f32 v0, v10, v11
	s_nop 0
	v_cndmask_b32_e32 v8, v152, v8, vcc
	v_cmp_nlt_f32_e32 vcc, s59, v9
	s_nop 1
	v_cndmask_b32_e32 v0, 0, v0, vcc
	v_cmp_ngt_f32_e32 vcc, s61, v9
	s_nop 1
	v_cndmask_b32_e32 v9, v152, v0, vcc
	v_pk_add_f32 v[8:9], v[8:9], 1.0 op_sel_hi:[1,0]
	s_nop 0
	v_div_scale_f32 v0, s[6:7], v9, v9, 1.0
	v_rcp_f32_e32 v10, v0
	s_nop 0
	v_fma_f32 v11, -v0, v10, 1.0
	v_fmac_f32_e32 v10, v11, v10
	v_div_scale_f32 v11, vcc, 1.0, v9, 1.0
	v_mul_f32_e32 v14, v11, v10
	v_fma_f32 v15, -v0, v14, v11
	v_fmac_f32_e32 v14, v15, v10
	v_fma_f32 v0, -v0, v14, v11
	v_div_scale_f32 v11, s[6:7], v8, v8, 1.0
	v_rcp_f32_e32 v15, v11
	v_div_fmas_f32 v0, v0, v10, v14
	s_waitcnt lgkmcnt(12)
	v_mov_b32_e32 v14, v24
	v_mul_f32_e32 v17, 0xbfb8aa3b, v14
	v_fma_f32 v18, v14, s58, -v17
	v_rndne_f32_e32 v19, v17
	v_fmac_f32_e32 v18, 0xb2a5705f, v14
	v_sub_f32_e32 v17, v17, v19
	v_div_fixup_f32 v9, v0, v9, 1.0
	v_fma_f32 v0, -v11, v15, 1.0
	v_add_f32_e32 v17, v17, v18
	v_fmac_f32_e32 v15, v0, v15
	v_div_scale_f32 v0, vcc, 1.0, v8, 1.0
	v_exp_f32_e32 v17, v17
	v_cvt_i32_f32_e32 v18, v19
	v_mul_f32_e32 v10, v0, v15
	v_fma_f32 v19, -v11, v10, v0
	v_fmac_f32_e32 v10, v19, v15
	v_fma_f32 v0, -v11, v10, v0
	v_ldexp_f32 v11, v17, v18
	v_cmp_nlt_f32_e64 s[6:7], s59, v14
	v_div_fmas_f32 v0, v0, v15, v10
	s_waitcnt lgkmcnt(12)
	v_mov_b32_e32 v15, v22
	v_cndmask_b32_e64 v11, 0, v11, s[6:7]
	v_cmp_ngt_f32_e64 s[6:7], s61, v14
	v_mul_f32_e32 v18, 0xbfb8aa3b, v15
	v_fma_f32 v19, v15, s58, -v18
	v_cndmask_b32_e64 v11, v152, v11, s[6:7]
	v_add_f32_e32 v11, 1.0, v11
	v_div_scale_f32 v14, s[6:7], v11, v11, 1.0
	v_rcp_f32_e32 v17, v14
	v_rndne_f32_e32 v20, v18
	v_fmac_f32_e32 v19, 0xb2a5705f, v15
	v_sub_f32_e32 v18, v18, v20
	v_div_fixup_f32 v8, v0, v8, 1.0
	v_fma_f32 v0, -v14, v17, 1.0
	v_add_f32_e32 v18, v18, v19
	v_fmac_f32_e32 v17, v0, v17
	v_div_scale_f32 v0, vcc, 1.0, v11, 1.0
	v_exp_f32_e32 v18, v18
	v_cvt_i32_f32_e32 v19, v20
	v_mul_f32_e32 v10, v0, v17
	v_fma_f32 v20, -v14, v10, v0
	v_fmac_f32_e32 v10, v20, v17
	v_fma_f32 v0, -v14, v10, v0
	v_ldexp_f32 v14, v18, v19
	v_cmp_nlt_f32_e64 s[6:7], s59, v15
	v_div_fmas_f32 v0, v0, v17, v10
	v_div_fixup_f32 v0, v0, v11, 1.0
	v_cndmask_b32_e64 v14, 0, v14, s[6:7]
	v_cmp_ngt_f32_e64 s[6:7], s61, v15
	v_pk_add_f32 v[4:5], v[4:5], v[8:9]
	v_add_f32_e32 v6, v6, v0
	v_cndmask_b32_e64 v14, v152, v14, s[6:7]
	v_add_f32_e32 v14, 1.0, v14
	v_div_scale_f32 v15, s[6:7], v14, v14, 1.0
	v_rcp_f32_e32 v18, v15
	v_cmp_nlg_f32_e64 s[8:9], s62, v4
	v_fma_f32 v10, -v15, v18, 1.0
	v_fmac_f32_e32 v18, v10, v18
	v_div_scale_f32 v10, vcc, 1.0, v14, 1.0
	v_mul_f32_e32 v11, v10, v18
	v_fma_f32 v17, -v15, v11, v10
	v_fmac_f32_e32 v11, v17, v18
	v_fma_f32 v10, -v15, v11, v10
	v_div_fmas_f32 v10, v10, v18, v11
	v_cmp_gt_f32_e32 vcc, v5, v4
	v_div_fixup_f32 v10, v10, v14, 1.0
	v_add_f32_e32 v7, v7, v10
	v_cndmask_b32_e32 v15, v4, v5, vcc
	v_cndmask_b32_e32 v11, v8, v9, vcc
	v_cndmask_b32_e64 v14, 0, 1, vcc
	v_cmp_gt_f32_e32 vcc, v6, v15
	s_nop 1
	v_cndmask_b32_e32 v15, v15, v6, vcc
	v_cndmask_b32_e32 v11, v11, v0, vcc
	v_cndmask_b32_e64 v14, v14, 2, vcc
	v_cmp_ngt_f32_e32 vcc, v7, v15
	s_nop 1
	v_cndmask_b32_e32 v14, 3, v14, vcc
	v_cmp_eq_u32_e64 s[6:7], 0, v14
	s_or_b64 s[6:7], s[6:7], s[8:9]
	v_cndmask_b32_e32 v11, v10, v11, vcc
	v_cndmask_b32_e64 v4, v4, v153, s[6:7]
	v_cndmask_b32_e64 v8, v8, 0, s[6:7]
	v_cmp_ne_u32_e64 s[6:7], 1, v14
	v_cmp_gt_f32_e64 s[8:9], v5, v4
	s_and_b64 s[6:7], s[6:7], s[8:9]
	v_cndmask_b32_e64 v4, v4, v5, s[6:7]
	v_cmp_ne_u32_e64 s[8:9], 2, v14
	v_cmp_gt_f32_e64 s[10:11], v6, v4
	s_and_b64 s[8:9], s[8:9], s[10:11]
	v_cndmask_b32_e64 v4, v4, v6, s[8:9]
	v_cmp_gt_f32_e64 s[10:11], v7, v4
	v_cndmask_b32_e32 v15, v7, v15, vcc
	s_and_b64 vcc, vcc, s[10:11]
	v_cndmask_b32_e64 v5, v8, v9, s[6:7]
	v_cndmask_b32_e32 v4, v4, v7, vcc
	v_cndmask_b32_e64 v0, v5, v0, s[8:9]
	v_add_f32_e32 v4, v15, v4
	v_cndmask_b32_e32 v0, v0, v10, vcc
	v_cndmask_b32_e64 v6, 12, 13, s[6:7]
	v_cmp_gt_f32_e64 s[6:7], v4, v16
	v_cndmask_b32_e64 v6, v6, 14, s[8:9]
	v_or_b32_e32 v5, 12, v14
	v_cndmask_b32_e64 v7, v3, v11, s[6:7]
	v_cndmask_b32_e64 v0, v13, v0, s[6:7]
	v_add_f32_e32 v9, v7, v0
	v_div_scale_f32 v8, s[8:9], v9, v9, v0
	v_rcp_f32_e32 v10, v8
	v_cndmask_b32_e64 v3, v6, 15, vcc
	v_cndmask_b32_e64 v4, v1, v3, s[6:7]
	v_cndmask_b32_e64 v3, v12, v5, s[6:7]
	v_fma_f32 v1, -v8, v10, 1.0
	v_fmac_f32_e32 v10, v1, v10
	v_div_scale_f32 v1, vcc, v0, v9, v0
	v_mul_f32_e32 v5, v1, v10
	v_fma_f32 v6, -v8, v5, v1
	v_fmac_f32_e32 v5, v6, v10
	v_div_scale_f32 v6, s[6:7], v9, v9, v7
	v_rcp_f32_e32 v11, v6
	v_fma_f32 v1, -v8, v5, v1
	v_div_fmas_f32 v1, v1, v10, v5
	v_div_fixup_f32 v8, v1, v9, v0
	v_fma_f32 v0, -v6, v11, 1.0
	v_fmac_f32_e32 v11, v0, v11
	v_div_scale_f32 v0, vcc, v7, v9, v7
	v_mul_f32_e32 v1, v0, v11
	v_fma_f32 v5, -v6, v1, v0
	v_fmac_f32_e32 v1, v5, v11
	v_fma_f32 v0, -v6, v1, v0
	v_div_fmas_f32 v0, v0, v11, v1
	v_lshl_add_u32 v1, v3, 2, s63
	ds_add_rtn_u32 v5, v1, v151
	v_lshl_add_u32 v1, v4, 2, s63
	ds_add_rtn_u32 v6, v1, v151
	v_div_fixup_f32 v7, v0, v9, v7
	v_add_u32_e32 v0, 1, v154
	v_lshl_add_u32 v1, v154, 8, v85
	v_mov_b32_e32 v154, v0
	s_waitcnt lgkmcnt(1)
	ds_write_b128 v1, v[2:5]
	s_waitcnt lgkmcnt(1)
	ds_write_b96 v1, v[6:8] offset:16
	s_branch .LBB0_520
